# attention softmax: running max folded into the QK accumulator start (C=-m), per-element subtraction only when a row max grows past the defer threshold; f32 throughout; on top of v22
# speedup vs baseline: 1.0093x; 1.0093x over previous
.LBB0_804:
	s_bfe_u32 s0, s66, 0x20001
	s_bfe_u32 s1, s78, 0x10007
	s_lshl_b32 s12, s1, 8
	s_lshl_b32 s44, s0, 9
	s_or_b32 s48, s44, s12
	s_mulk_i32 s0, 0x180
	s_mul_i32 s12, s1, 0xc0
	s_add_i32 s0, s0, s12
	s_lshl_b32 s50, s0, 1
	s_ashr_i32 s0, s78, 4
	s_lshl_b32 s12, s78, 1
	s_and_b32 s0, s0, -16
	s_and_b32 s44, s12, 8
	s_bfe_u32 s80, s78, 0x40003
	s_or_b32 s0, s0, s44
	s_xor_b32 s49, s80, 31
	s_ashr_i32 s0, s0, 3
	s_and_b32 s12, s12, 6
	s_lshl_b32 s83, s49, 8
	s_or_b32 s46, s12, s1
	s_ashr_i32 s1, s0, 31
	s_add_i32 s84, s83, s63
	s_lshr_b32 s81, s78, 3
	v_mov_b32_e32 v172, v1
	s_lshl_b64 s[52:53], s[0:1], 13
	s_ashr_i32 s12, s84, 31
	s_add_u32 s54, s52, s84
	v_and_b32_e32 v168, 31, v172
	v_or_b32_e32 v38, s54, v168
	s_addc_u32 s55, s53, s12
	v_mad_u64_u32 v[2:3], s[44:45], v38, s68, v[146:147]
	s_mul_i32 s82, s46, 0xc0
	v_bfe_u32 v173, v172, 5, 1
	v_mad_i32_i24 v3, s55, v162, v3
	s_lshl_b32 s12, s82, 1
	v_lshl_add_u64 v[2:3], v[2:3], 0, s[12:13]
	v_lshlrev_b32_e32 v148, 4, v173
	v_lshl_add_u64 v[40:41], v[2:3], 0, v[148:149]
	global_load_dwordx4 v[6:9], v[40:41], off
	global_load_dwordx4 v[14:17], v[40:41], off offset:32
	global_load_dwordx4 v[30:33], v[40:41], off offset:64
	global_load_dwordx4 v[34:37], v[40:41], off offset:96
	global_load_dwordx4 v[50:53], v[40:41], off offset:128
	global_load_dwordx4 v[26:29], v[40:41], off offset:160
	global_load_dwordx4 v[22:25], v[40:41], off offset:192
	global_load_dwordx4 v[18:21], v[40:41], off offset:224
	global_load_dwordx4 v[10:13], v[40:41], off offset:256
	global_load_dwordx4 v[42:45], v[40:41], off offset:288
	s_waitcnt lgkmcnt(0)
	global_load_dwordx4 v[2:5], v[40:41], off offset:320
	global_load_dwordx4 v[46:49], v[40:41], off offset:352
	v_and_b32_e32 v40, 32, v172
	v_mov_b32_e32 v39, s55
	s_mul_i32 s86, s0, 0x1800000
	s_mul_hi_i32 s51, s0, 0x1800000
	s_add_u32 s44, s33, s86
	s_addc_u32 s45, s58, s51
	s_lshl_b64 s[56:57], s[0:1], 24
	s_lshl_b32 s79, s46, 7
	s_add_u32 s44, s44, s12
	s_addc_u32 s45, s45, 0
	s_mov_b32 m0, s71
	s_add_u32 s0, s59, s56
	s_addc_u32 s1, s60, s57
	s_lshl_b32 s12, s46, 8
	s_add_u32 s46, s0, s12
	s_addc_u32 s47, s1, 0
	s_lshl_b32 s85, s49, 2
	s_add_i32 s85, s85, 4
	s_or_b32 s48, s56, s48
	s_add_u32 s48, s48, 0x29020000
	s_addc_u32 s49, s57, 0
	s_or_b32 s50, s86, s50
	s_add_u32 s50, s50, 0x23030000
	s_addc_u32 s51, s51, 0
	s_mov_b32 s12, 1
	s_movk_i32 s86, 0xff00
	s_waitcnt vmcnt(0)
	v_lshlrev_b32_e32 v227, 16, v26
	v_lshlrev_b32_e32 v177, 16, v6
	v_and_b32_e32 v174, 0xffff0000, v6
	v_lshlrev_b32_e32 v170, 16, v7
	v_and_b32_e32 v167, 0xffff0000, v7
	v_lshlrev_b32_e32 v180, 16, v8
	v_and_b32_e32 v176, 0xffff0000, v8
	v_lshlrev_b32_e32 v171, 16, v9
	v_and_b32_e32 v169, 0xffff0000, v9
	v_lshlrev_b32_e32 v185, 16, v14
	v_and_b32_e32 v182, 0xffff0000, v14
	v_lshlrev_b32_e32 v179, 16, v15
	v_and_b32_e32 v175, 0xffff0000, v15
	v_lshlrev_b32_e32 v187, 16, v16
	v_and_b32_e32 v183, 0xffff0000, v16
	v_lshlrev_b32_e32 v181, 16, v17
	v_and_b32_e32 v178, 0xffff0000, v17
	v_lshlrev_b32_e32 v201, 16, v34
	v_and_b32_e32 v198, 0xffff0000, v34
	v_lshlrev_b32_e32 v196, 16, v35
	v_and_b32_e32 v192, 0xffff0000, v35
	v_lshlrev_b32_e32 v202, 16, v36
	v_and_b32_e32 v199, 0xffff0000, v36
	v_lshlrev_b32_e32 v197, 16, v37
	v_and_b32_e32 v194, 0xffff0000, v37
	v_and_b32_e32 v228, 0xffff0000, v26
	global_load_dwordx4 v[142:145], v40, s[4:5] offset:704
	global_load_dwordx4 v[130:133], v40, s[4:5] offset:720
	global_load_dwordx4 v[6:9], v40, s[4:5] offset:592
	v_lshlrev_b32_e32 v229, 16, v27
	global_load_dwordx4 v[14:17], v40, s[4:5] offset:576
	v_and_b32_e32 v230, 0xffff0000, v27
	v_lshlrev_b32_e32 v231, 16, v28
	v_and_b32_e32 v232, 0xffff0000, v28
	v_lshlrev_b32_e32 v233, 16, v29
	v_and_b32_e32 v234, 0xffff0000, v29
	global_load_dwordx4 v[34:37], v40, s[4:5] offset:640
	global_load_dwordx4 v[156:159], v40, s[4:5] offset:656
	global_load_dwordx4 v[26:29], v40, s[4:5] offset:528
	v_mul_f32_e32 v209, v174, v174
	v_fmac_f32_e32 v209, v177, v177
	v_fmac_f32_e32 v209, v170, v170
	v_fmac_f32_e32 v209, v167, v167
	v_fmac_f32_e32 v209, v180, v180
	v_fmac_f32_e32 v209, v176, v176
	v_fmac_f32_e32 v209, v171, v171
	v_fmac_f32_e32 v209, v169, v169
	v_fmac_f32_e32 v209, v185, v185
	v_lshlrev_b32_e32 v193, 16, v30
	v_and_b32_e32 v190, 0xffff0000, v30
	v_lshlrev_b32_e32 v188, 16, v31
	v_and_b32_e32 v184, 0xffff0000, v31
	v_lshlrev_b32_e32 v195, 16, v32
	v_and_b32_e32 v191, 0xffff0000, v32
	v_lshlrev_b32_e32 v189, 16, v33
	v_and_b32_e32 v186, 0xffff0000, v33
	v_fmac_f32_e32 v209, v182, v182
	global_load_dwordx4 v[30:33], v40, s[4:5] offset:512
	v_fmac_f32_e32 v209, v179, v179
	v_fmac_f32_e32 v209, v175, v175
	v_fmac_f32_e32 v209, v187, v187
	v_fmac_f32_e32 v209, v183, v183
	v_fmac_f32_e32 v209, v181, v181
	v_fmac_f32_e32 v209, v178, v178
	v_fmac_f32_e32 v209, v193, v193
	v_fmac_f32_e32 v209, v190, v190
	v_fmac_f32_e32 v209, v188, v188
	v_fmac_f32_e32 v209, v184, v184
	v_fmac_f32_e32 v209, v195, v195
	v_fmac_f32_e32 v209, v191, v191
	v_fmac_f32_e32 v209, v189, v189
	v_fmac_f32_e32 v209, v186, v186
	v_fmac_f32_e32 v209, v201, v201
	v_fmac_f32_e32 v209, v198, v198
	v_fmac_f32_e32 v209, v196, v196
	v_fmac_f32_e32 v209, v192, v192
	v_fmac_f32_e32 v209, v202, v202
	v_fmac_f32_e32 v209, v199, v199
	v_fmac_f32_e32 v209, v197, v197
	v_lshlrev_b32_e32 v207, 16, v50
	v_fmac_f32_e32 v209, v194, v194
	v_and_b32_e32 v205, 0xffff0000, v50
	v_fmac_f32_e32 v209, v207, v207
	v_lshlrev_b32_e32 v203, 16, v51
	v_fmac_f32_e32 v209, v205, v205
	v_and_b32_e32 v200, 0xffff0000, v51
	v_fmac_f32_e32 v209, v203, v203
	v_lshlrev_b32_e32 v208, 16, v52
	v_fmac_f32_e32 v209, v200, v200
	v_and_b32_e32 v206, 0xffff0000, v52
	v_fmac_f32_e32 v209, v208, v208
	v_lshlrev_b32_e32 v204, 16, v53
	v_fmac_f32_e32 v209, v206, v206
	v_and_b32_e32 v226, 0xffff0000, v53
	v_fmac_f32_e32 v209, v204, v204
	v_fmac_f32_e32 v209, v226, v226
	v_fmac_f32_e32 v209, v227, v227
	v_fmac_f32_e32 v209, v228, v228
	v_fmac_f32_e32 v209, v229, v229
	v_fmac_f32_e32 v209, v230, v230
	global_load_dwordx4 v[110:113], v40, s[4:5] offset:16
	global_load_dwordx4 v[114:117], v40, s[4:5]
	global_load_dwordx4 v[102:105], v40, s[4:5] offset:80
	global_load_dwordx4 v[106:109], v40, s[4:5] offset:64
	global_load_dwordx4 v[94:97], v40, s[4:5] offset:144
	global_load_dwordx4 v[98:101], v40, s[4:5] offset:128
	global_load_dwordx4 v[86:89], v40, s[4:5] offset:208
	global_load_dwordx4 v[90:93], v40, s[4:5] offset:192
	global_load_dwordx4 v[78:81], v40, s[4:5] offset:272
	global_load_dwordx4 v[82:85], v40, s[4:5] offset:256
	global_load_dwordx4 v[70:73], v40, s[4:5] offset:336
	global_load_dwordx4 v[74:77], v40, s[4:5] offset:320
	global_load_dwordx4 v[62:65], v40, s[4:5] offset:400
	global_load_dwordx4 v[66:69], v40, s[4:5] offset:384
	global_load_dwordx4 v[54:57], v40, s[4:5] offset:464
	global_load_dwordx4 v[58:61], v40, s[4:5] offset:448
	v_fmac_f32_e32 v209, v231, v231
	v_fmac_f32_e32 v209, v232, v232
	v_fmac_f32_e32 v209, v233, v233
	v_fmac_f32_e32 v209, v234, v234
	s_waitcnt vmcnt(29)
	v_lshlrev_b32_e32 v235, 16, v22
	v_and_b32_e32 v236, 0xffff0000, v22
	v_fmac_f32_e32 v209, v235, v235
	v_lshlrev_b32_e32 v237, 16, v23
	v_fmac_f32_e32 v209, v236, v236
	v_and_b32_e32 v238, 0xffff0000, v23
	v_fmac_f32_e32 v209, v237, v237
	v_lshlrev_b32_e32 v239, 16, v24
	v_fmac_f32_e32 v209, v238, v238
	v_and_b32_e32 v240, 0xffff0000, v24
	v_fmac_f32_e32 v209, v239, v239
	v_lshlrev_b32_e32 v241, 16, v25
	v_fmac_f32_e32 v209, v240, v240
	v_and_b32_e32 v242, 0xffff0000, v25
	v_fmac_f32_e32 v209, v241, v241
	v_fmac_f32_e32 v209, v242, v242
	s_waitcnt vmcnt(28)
	v_lshlrev_b32_e32 v243, 16, v18
	v_and_b32_e32 v244, 0xffff0000, v18
	v_fmac_f32_e32 v209, v243, v243
	v_lshlrev_b32_e32 v245, 16, v19
	v_fmac_f32_e32 v209, v244, v244
	v_and_b32_e32 v246, 0xffff0000, v19
	v_fmac_f32_e32 v209, v245, v245
	v_lshlrev_b32_e32 v247, 16, v20
	v_fmac_f32_e32 v209, v246, v246
	v_and_b32_e32 v248, 0xffff0000, v20
	v_fmac_f32_e32 v209, v247, v247
	v_lshlrev_b32_e32 v249, 16, v21
	v_fmac_f32_e32 v209, v248, v248
	v_and_b32_e32 v250, 0xffff0000, v21
	v_fmac_f32_e32 v209, v249, v249
	s_waitcnt vmcnt(27)
	v_lshlrev_b32_e32 v223, 16, v10
	s_waitcnt vmcnt(25)
	v_lshlrev_b32_e32 v222, 16, v2
	v_fmac_f32_e32 v209, v250, v250
	s_waitcnt vmcnt(18)
	v_mov_b32_e32 v150, v158
	v_mov_b32_e32 v158, v156
	v_lshlrev_b32_e32 v156, 16, v3
	v_and_b32_e32 v160, 0xffff0000, v3
	v_and_b32_e32 v225, 0xffff0000, v10
	v_and_b32_e32 v224, 0xffff0000, v2
	v_pk_mul_f32 v[2:3], v[222:223], v[222:223]
	v_mov_b32_e32 v134, v144
	v_mov_b32_e32 v140, v142
	v_lshlrev_b32_e32 v142, 16, v5
	s_waitcnt vmcnt(17)
	v_mov_b32_e32 v151, v28
	v_and_b32_e32 v144, 0xffff0000, v5
	v_mov_b32_e32 v28, v159
	v_lshlrev_b32_e32 v152, 16, v4
	v_mov_b32_e32 v159, v26
	v_and_b32_e32 v154, 0xffff0000, v4
	v_mov_b32_e32 v26, v157
	v_lshlrev_b32_e32 v157, 16, v11
	v_add_f32_e32 v3, v3, v209
	v_pk_mul_f32 v[4:5], v[224:225], v[224:225]
	v_lshlrev_b32_e32 v119, 16, v45
	v_and_b32_e32 v121, 0xffff0000, v45
	v_lshlrev_b32_e32 v125, 16, v44
	v_and_b32_e32 v127, 0xffff0000, v44
	v_pk_mul_f32 v[44:45], v[156:157], v[156:157]
	v_and_b32_e32 v161, 0xffff0000, v11
	v_add_f32_e32 v3, v5, v3
	v_mov_b32_e32 v122, v132
	v_mov_b32_e32 v128, v130
	v_lshlrev_b32_e32 v130, 16, v47
	v_and_b32_e32 v132, 0xffff0000, v47
	v_lshlrev_b32_e32 v136, 16, v46
	v_and_b32_e32 v138, 0xffff0000, v46
	v_lshlrev_b32_e32 v153, 16, v12
	v_pk_mul_f32 v[46:47], v[160:161], v[160:161]
	v_add_f32_e32 v3, v45, v3
	v_mov_b32_e32 v123, v8
	v_mov_b32_e32 v8, v133
	v_mov_b32_e32 v129, v6
	v_mov_b32_e32 v6, v131
	v_lshlrev_b32_e32 v131, 16, v43
	v_and_b32_e32 v133, 0xffff0000, v43
	v_lshlrev_b32_e32 v137, 16, v42
	v_and_b32_e32 v139, 0xffff0000, v42
	v_pk_mul_f32 v[42:43], v[152:153], v[152:153]
	v_and_b32_e32 v155, 0xffff0000, v12
	v_add_f32_e32 v3, v47, v3
	v_mov_b32_e32 v141, v14
	v_mov_b32_e32 v14, v143
	v_lshlrev_b32_e32 v143, 16, v13
	v_pk_mul_f32 v[220:221], v[154:155], v[154:155]
	v_add_f32_e32 v3, v43, v3
	v_mov_b32_e32 v135, v16
	v_mov_b32_e32 v16, v145
	v_pk_mul_f32 v[216:217], v[142:143], v[142:143]
	v_and_b32_e32 v145, 0xffff0000, v13
	v_add_f32_e32 v3, v221, v3
	v_pk_mul_f32 v[218:219], v[144:145], v[144:145]
	v_add_f32_e32 v3, v217, v3
	v_pk_mul_f32 v[212:213], v[136:137], v[136:137]
	v_add_f32_e32 v3, v219, v3
	v_pk_mul_f32 v[214:215], v[138:139], v[138:139]
	v_add_f32_e32 v3, v213, v3
	v_add_f32_e32 v3, v215, v3
	v_fmac_f32_e32 v3, v131, v131
	v_fmac_f32_e32 v3, v133, v133
	v_fmac_f32_e32 v3, v125, v125
	v_fmac_f32_e32 v3, v127, v127
	v_fmac_f32_e32 v3, v119, v119
	v_fmac_f32_e32 v3, v121, v121
	v_add_f32_e32 v2, v2, v3
	v_add_f32_e32 v43, v4, v2
	v_add_f32_e32 v43, v44, v43
	v_add_f32_e32 v43, v46, v43
	v_add_f32_e32 v209, v42, v43
	v_add_f32_e32 v209, v220, v209
	v_add_f32_e32 v209, v216, v209
	v_add_f32_e32 v209, v218, v209
	v_mov_b32_e32 v218, v132
	v_mov_b32_e32 v219, v130
	v_add_f32_e32 v209, v212, v209
	v_lshlrev_b64 v[18:19], 8, v[38:39]
	v_lshlrev_b32_e32 v124, 16, v48
	v_and_b32_e32 v126, 0xffff0000, v48
	v_pk_mul_f32 v[218:219], v[218:219], v[218:219]
	s_waitcnt vmcnt(16)
	v_mov_b32_e32 v213, v32
	v_add_f32_e32 v32, v214, v209
	v_lshl_add_u64 v[18:19], s[10:11], 0, v[18:19]
	v_lshlrev_b32_e32 v20, 6, v173
	v_mov_b32_e32 v21, v149
	v_mov_b32_e32 v216, v126
	v_mov_b32_e32 v217, v124
	v_add_f32_e32 v32, v219, v32
	v_lshl_add_u64 v[210:211], v[18:19], 0, v[20:21]
	v_lshlrev_b32_e32 v118, 16, v49
	v_and_b32_e32 v120, 0xffff0000, v49
	v_pk_mul_f32 v[216:217], v[216:217], v[216:217]
	v_add_f32_e32 v32, v218, v32
	global_load_dwordx4 v[18:21], v[210:211], off offset:48
	global_load_dwordx4 v[22:25], v[210:211], off offset:32
	global_load_dwordx4 v[38:41], v[210:211], off offset:16
	global_load_dwordx4 v[50:53], v[210:211], off
	global_load_dwordx4 v[2:5], v[210:211], off offset:176
	global_load_dwordx4 v[10:13], v[210:211], off offset:160
	global_load_dwordx4 v[42:45], v[210:211], off offset:144
	global_load_dwordx4 v[46:49], v[210:211], off offset:128
	v_mov_b32_e32 v210, v120
	v_mov_b32_e32 v211, v118
	v_add_f32_e32 v32, v217, v32
	v_pk_mul_f32 v[210:211], v[210:211], v[210:211]
	v_add_f32_e32 v32, v216, v32
	v_add_f32_e32 v32, v211, v32
	v_add_f32_e32 v32, v210, v32
	v_mov_b32_e32 v212, v36
	v_mov_b32_e32 v36, v32
	s_nop 1
	v_permlane32_swap_b32_e32 v32, v36
	v_add_f32_e32 v32, v32, v36
	v_fmamk_f32 v32, v32, 0x3baaaaab, v163
	v_mul_f32_e32 v36, 0x4b800000, v32
	v_cmp_gt_f32_e32 vcc, s69, v32
	s_nop 1
	v_cndmask_b32_e32 v32, v32, v36, vcc
	v_rsq_f32_e32 v209, v32
	v_mov_b32_e32 v32, v37
	v_mov_b32_e32 v37, v30
	v_mov_b32_e32 v36, v34
	v_mul_f32_e32 v30, 0x45800000, v209
	v_cndmask_b32_e32 v30, v209, v30, vcc
	v_mul_f32_e32 v34, 0x3dd53b94, v30
	s_waitcnt vmcnt(22)
	v_mul_f32_e32 v30, v114, v34
	v_mul_f32_e32 v114, v30, v177
	v_mul_f32_e32 v30, v110, v34
	v_mul_f32_e32 v110, v30, v180
	v_mul_f32_e32 v30, v115, v34
	v_mul_f32_e32 v115, v30, v174
	v_mul_f32_e32 v30, v111, v34
	v_mul_f32_e32 v111, v30, v176
	v_mul_f32_e32 v30, v116, v34
	v_mul_f32_e32 v116, v30, v170
	v_mul_f32_e32 v30, v112, v34
	v_mul_f32_e32 v112, v30, v171
	v_mul_f32_e32 v30, v117, v34
	v_mul_f32_e32 v117, v30, v167
	v_mul_f32_e32 v30, v113, v34
	v_mul_f32_e32 v113, v30, v169
	s_waitcnt vmcnt(20)
	v_mul_f32_e32 v30, v106, v34
	v_mul_f32_e32 v106, v30, v185
	v_mul_f32_e32 v30, v102, v34
	v_mul_f32_e32 v167, v30, v187
	v_mul_f32_e32 v30, v107, v34
	v_mul_f32_e32 v102, v30, v182
	v_mul_f32_e32 v30, v103, v34
	v_mul_f32_e32 v107, v30, v183
	v_mul_f32_e32 v30, v108, v34
	v_mul_f32_e32 v103, v30, v179
	v_mul_f32_e32 v30, v104, v34
	v_mul_f32_e32 v108, v30, v181
	v_mul_f32_e32 v30, v109, v34
	v_mul_f32_e32 v104, v30, v175
	v_mul_f32_e32 v30, v105, v34
	v_mul_f32_e32 v105, v30, v178
	s_waitcnt vmcnt(18)
	v_mul_f32_e32 v30, v98, v34
	v_mul_f32_e32 v109, v30, v193
	v_mul_f32_e32 v30, v94, v34
	v_mul_f32_e32 v94, v30, v195
	v_mul_f32_e32 v30, v99, v34
	v_mul_f32_e32 v169, v30, v190
	v_mul_f32_e32 v30, v95, v34
	v_mul_f32_e32 v95, v30, v191
	v_mul_f32_e32 v30, v100, v34
	v_mul_f32_e32 v170, v30, v188
	v_mul_f32_e32 v30, v96, v34
	v_mul_f32_e32 v96, v30, v189
	v_mul_f32_e32 v30, v101, v34
	v_mul_f32_e32 v171, v30, v184
	v_mul_f32_e32 v30, v97, v34
	v_mul_f32_e32 v97, v30, v186
	s_waitcnt vmcnt(16)
	v_mul_f32_e32 v30, v90, v34
	v_mul_f32_e32 v90, v30, v201
	v_mul_f32_e32 v30, v86, v34
	v_mul_f32_e32 v86, v30, v202
	v_mul_f32_e32 v30, v91, v34
	v_mul_f32_e32 v91, v30, v198
	v_mul_f32_e32 v30, v87, v34
	v_mul_f32_e32 v87, v30, v199
	v_mul_f32_e32 v30, v92, v34
	v_mul_f32_e32 v92, v30, v196
	v_mul_f32_e32 v30, v88, v34
	v_mul_f32_e32 v88, v30, v197
	v_mul_f32_e32 v30, v93, v34
	v_mul_f32_e32 v93, v30, v192
	v_mul_f32_e32 v30, v89, v34
	v_mul_f32_e32 v89, v30, v194
	s_waitcnt vmcnt(14)
	v_mul_f32_e32 v30, v82, v34
	v_mul_f32_e32 v82, v30, v207
	v_mul_f32_e32 v30, v34, v78
	v_mul_f32_e32 v78, v30, v208
	v_mul_f32_e32 v30, v83, v34
	v_mul_f32_e32 v83, v30, v205
	v_mul_f32_e32 v30, v34, v79
	v_mul_f32_e32 v79, v30, v206
	v_mul_f32_e32 v30, v84, v34
	v_mul_f32_e32 v84, v30, v203
	v_mul_f32_e32 v30, v34, v80
	v_mul_f32_e32 v80, v30, v204
	v_mul_f32_e32 v30, v85, v34
	v_mul_f32_e32 v85, v30, v200
	v_mul_f32_e32 v30, v34, v81
	v_mul_f32_e32 v81, v30, v226
	s_waitcnt vmcnt(12)
	v_mul_f32_e32 v30, v34, v74
	v_mul_f32_e32 v74, v30, v227
	v_mul_f32_e32 v30, v34, v70
	v_mul_f32_e32 v70, v30, v231
	v_mul_f32_e32 v30, v34, v75
	v_mul_f32_e32 v75, v30, v228
	v_mul_f32_e32 v30, v34, v71
	v_mul_f32_e32 v71, v30, v232
	v_mul_f32_e32 v30, v34, v76
	v_mul_f32_e32 v76, v30, v229
	v_mul_f32_e32 v30, v34, v72
	v_mul_f32_e32 v72, v30, v233
	v_mul_f32_e32 v30, v34, v77
	v_mul_f32_e32 v77, v30, v230
	v_mul_f32_e32 v30, v34, v73
	v_mul_f32_e32 v73, v30, v234
	s_waitcnt vmcnt(10)
	v_mul_f32_e32 v30, v34, v66
	v_mul_f32_e32 v174, v30, v235
	v_mul_f32_e32 v30, v34, v62
	v_mul_f32_e32 v175, v30, v239
	v_mul_f32_e32 v30, v34, v67
	v_mul_f32_e32 v176, v30, v236
	v_mul_f32_e32 v30, v34, v63
	v_mul_f32_e32 v177, v30, v240
	v_mul_f32_e32 v30, v34, v68
	v_mul_f32_e32 v68, v30, v237
	v_mul_f32_e32 v30, v34, v64
	v_mul_f32_e32 v178, v30, v241
	v_mul_f32_e32 v30, v34, v69
	v_mul_f32_e32 v69, v30, v238
	v_mul_f32_e32 v30, v34, v65
	v_mul_f32_e32 v179, v30, v242
	s_waitcnt vmcnt(8)
	v_mul_f32_e32 v30, v34, v58
	v_mul_f32_e32 v180, v30, v243
	v_mul_f32_e32 v30, v34, v54
	v_mul_f32_e32 v181, v30, v247
	v_mul_f32_e32 v30, v34, v59
	v_mul_f32_e32 v182, v30, v244
	v_mul_f32_e32 v30, v34, v55
	v_mul_f32_e32 v183, v30, v248
	v_mul_f32_e32 v30, v34, v60
	v_mul_f32_e32 v184, v30, v245
	v_mul_f32_e32 v30, v34, v56
	v_mul_f32_e32 v185, v30, v249
	v_mul_f32_e32 v30, v34, v61
	v_mul_f32_e32 v186, v30, v246
	v_mul_f32_e32 v30, v34, v57
	v_pk_mul_f32 v[36:37], v[34:35], v[36:37] op_sel_hi:[0,1]
	v_mul_f32_e32 v187, v30, v250
	v_pk_mul_f32 v[36:37], v[36:37], v[222:223]
	v_mov_b32_e32 v30, v35
	v_pk_mul_f32 v[54:55], v[34:35], v[158:159] op_sel_hi:[0,1]
	v_pk_mul_f32 v[30:31], v[34:35], v[30:31] op_sel_hi:[0,1]
	v_pk_mul_f32 v[26:27], v[34:35], v[26:27] op_sel_hi:[0,1]
	v_pk_mul_f32 v[56:57], v[34:35], v[212:213] op_sel_hi:[0,1]
	v_pk_mul_f32 v[58:59], v[34:35], v[150:151] op_sel_hi:[0,1]
	v_pk_mul_f32 v[32:33], v[34:35], v[32:33] op_sel_hi:[0,1]
	v_pk_mul_f32 v[28:29], v[34:35], v[28:29] op_sel_hi:[0,1]
	v_pk_mul_f32 v[60:61], v[34:35], v[140:141] op_sel_hi:[0,1]
	v_pk_mul_f32 v[62:63], v[34:35], v[128:129] op_sel_hi:[0,1]
	v_pk_mul_f32 v[14:15], v[34:35], v[14:15] op_sel_hi:[0,1]
	v_pk_mul_f32 v[6:7], v[34:35], v[6:7] op_sel_hi:[0,1]
	v_pk_mul_f32 v[64:65], v[34:35], v[134:135] op_sel_hi:[0,1]
	v_pk_mul_f32 v[66:67], v[34:35], v[122:123] op_sel_hi:[0,1]
	v_pk_mul_f32 v[16:17], v[34:35], v[16:17] op_sel_hi:[0,1]
	v_pk_mul_f32 v[8:9], v[34:35], v[8:9] op_sel_hi:[0,1]
	s_waitcnt vmcnt(4)
	v_pk_mul_f32 v[34:35], v[36:37], v[50:51] op_sel:[1,0] op_sel_hi:[0,1]
	v_pk_mul_f32 v[30:31], v[30:31], v[224:225]
	v_pk_mul_f32 v[64:65], v[64:65], v[130:131]
	v_sub_f32_e32 v130, v34, v35
	v_pk_mul_f32 v[34:35], v[36:37], v[50:51]
	v_pk_mul_f32 v[56:57], v[56:57], v[156:157]
	v_add_f32_e32 v36, v35, v34
	v_pk_mul_f32 v[34:35], v[30:31], v[52:53] op_sel:[1,0] op_sel_hi:[0,1]
	v_pk_mul_f32 v[30:31], v[30:31], v[52:53]
	v_sub_f32_e32 v34, v34, v35
	v_add_f32_e32 v35, v31, v30
	v_pk_mul_f32 v[30:31], v[56:57], v[38:39] op_sel:[1,0] op_sel_hi:[0,1]
	v_pk_mul_f32 v[32:33], v[32:33], v[160:161]
	v_sub_f32_e32 v37, v30, v31
	v_pk_mul_f32 v[30:31], v[56:57], v[38:39]
	v_pk_mul_f32 v[54:55], v[54:55], v[152:153]
	v_add_f32_e32 v38, v31, v30
	v_pk_mul_f32 v[30:31], v[32:33], v[40:41] op_sel:[1,0] op_sel_hi:[0,1]
	v_sub_f32_e32 v39, v30, v31
	v_pk_mul_f32 v[30:31], v[32:33], v[40:41]
	v_pk_mul_f32 v[26:27], v[26:27], v[154:155]
	v_add_f32_e32 v32, v31, v30
	v_pk_mul_f32 v[30:31], v[54:55], v[22:23] op_sel:[1,0] op_sel_hi:[0,1]
	v_pk_mul_f32 v[22:23], v[54:55], v[22:23]
	v_sub_f32_e32 v30, v30, v31
	v_add_f32_e32 v31, v23, v22
	v_pk_mul_f32 v[22:23], v[26:27], v[24:25] op_sel:[1,0] op_sel_hi:[0,1]
	v_pk_mul_f32 v[58:59], v[58:59], v[142:143]
	v_sub_f32_e32 v33, v22, v23
	v_pk_mul_f32 v[22:23], v[26:27], v[24:25]
	v_pk_mul_f32 v[28:29], v[28:29], v[144:145]
	v_add_f32_e32 v24, v23, v22
	v_pk_mul_f32 v[22:23], v[58:59], v[18:19] op_sel:[1,0] op_sel_hi:[0,1]
	v_pk_mul_f32 v[18:19], v[58:59], v[18:19]
	v_sub_f32_e32 v22, v22, v23
	v_add_f32_e32 v23, v19, v18
	v_pk_mul_f32 v[18:19], v[28:29], v[20:21] op_sel:[1,0] op_sel_hi:[0,1]
	v_pk_mul_f32 v[60:61], v[60:61], v[136:137]
	v_sub_f32_e32 v25, v18, v19
	v_pk_mul_f32 v[18:19], v[28:29], v[20:21]
	v_pk_mul_f32 v[14:15], v[14:15], v[138:139]
	v_add_f32_e32 v20, v19, v18
	s_waitcnt vmcnt(0)
	v_pk_mul_f32 v[18:19], v[60:61], v[46:47] op_sel:[1,0] op_sel_hi:[0,1]
	v_sub_f32_e32 v21, v18, v19
	v_pk_mul_f32 v[18:19], v[60:61], v[46:47]
	v_pk_mul_f32 v[16:17], v[16:17], v[132:133]
	v_add_f32_e32 v26, v19, v18
	v_pk_mul_f32 v[18:19], v[14:15], v[48:49] op_sel:[1,0] op_sel_hi:[0,1]
	v_pk_mul_f32 v[14:15], v[14:15], v[48:49]
	v_sub_f32_e32 v18, v18, v19
	v_add_f32_e32 v19, v15, v14
	v_pk_mul_f32 v[14:15], v[64:65], v[42:43] op_sel:[1,0] op_sel_hi:[0,1]
	v_sub_f32_e32 v27, v14, v15
	v_pk_mul_f32 v[14:15], v[64:65], v[42:43]
	v_pk_mul_f32 v[62:63], v[62:63], v[124:125]
	v_add_f32_e32 v28, v15, v14
	v_pk_mul_f32 v[14:15], v[16:17], v[44:45] op_sel:[1,0] op_sel_hi:[0,1]
	v_sub_f32_e32 v29, v14, v15
	v_pk_mul_f32 v[14:15], v[16:17], v[44:45]
	v_pk_mul_f32 v[6:7], v[6:7], v[126:127]
	v_add_f32_e32 v16, v15, v14
	v_pk_mul_f32 v[14:15], v[62:63], v[10:11] op_sel:[1,0] op_sel_hi:[0,1]
	v_pk_mul_f32 v[10:11], v[62:63], v[10:11]
	v_pk_mul_f32 v[66:67], v[66:67], v[118:119]
	v_sub_f32_e32 v14, v14, v15
	v_add_f32_e32 v15, v11, v10
	v_pk_mul_f32 v[10:11], v[6:7], v[12:13] op_sel:[1,0] op_sel_hi:[0,1]
	v_pk_mul_f32 v[6:7], v[6:7], v[12:13]
	v_pk_mul_f32 v[8:9], v[8:9], v[120:121]
	v_sub_f32_e32 v10, v10, v11
	v_add_f32_e32 v11, v7, v6
	v_pk_mul_f32 v[6:7], v[66:67], v[2:3] op_sel:[1,0] op_sel_hi:[0,1]
	v_pk_mul_f32 v[2:3], v[66:67], v[2:3]
	v_sub_f32_e32 v6, v6, v7
	v_add_f32_e32 v7, v3, v2
	v_pk_mul_f32 v[2:3], v[8:9], v[4:5] op_sel:[1,0] op_sel_hi:[0,1]
	v_sub_f32_e32 v12, v2, v3
	v_pk_mul_f32 v[2:3], v[8:9], v[4:5]
	v_cvt_pk_bf16_f32 v98, v114, v115
	v_cvt_pk_bf16_f32 v99, v116, v117
	v_cvt_pk_bf16_f32 v100, v110, v111
	v_cvt_pk_bf16_f32 v101, v112, v113
	v_cvt_pk_bf16_f32 v102, v106, v102
	s_nop 0
	v_add_f32_e32 v2, v3, v2
	v_cvt_pk_bf16_f32 v103, v103, v104
	v_cvt_pk_bf16_f32 v104, v167, v107
	v_cvt_pk_bf16_f32 v105, v108, v105
	v_cvt_pk_bf16_f32 v106, v109, v169
	v_cvt_pk_bf16_f32 v107, v170, v171
	v_cvt_pk_bf16_f32 v108, v94, v95
	v_cvt_pk_bf16_f32 v109, v96, v97
	v_cvt_pk_bf16_f32 v110, v90, v91
	v_cvt_pk_bf16_f32 v111, v92, v93
	v_cvt_pk_bf16_f32 v112, v86, v87
	v_cvt_pk_bf16_f32 v113, v88, v89
	v_cvt_pk_bf16_f32 v114, v82, v83
	v_cvt_pk_bf16_f32 v115, v84, v85
	v_cvt_pk_bf16_f32 v116, v78, v79
	v_cvt_pk_bf16_f32 v117, v80, v81
	v_cvt_pk_bf16_f32 v118, v74, v75
	v_cvt_pk_bf16_f32 v119, v76, v77
	v_cvt_pk_bf16_f32 v120, v70, v71
	v_cvt_pk_bf16_f32 v121, v72, v73
	v_cvt_pk_bf16_f32 v122, v174, v176
	v_cvt_pk_bf16_f32 v123, v68, v69
	v_cvt_pk_bf16_f32 v124, v175, v177
	v_cvt_pk_bf16_f32 v125, v178, v179
	v_cvt_pk_bf16_f32 v126, v180, v182
	v_cvt_pk_bf16_f32 v127, v184, v186
	v_cvt_pk_bf16_f32 v128, v181, v183
	v_cvt_pk_bf16_f32 v129, v185, v187
	v_cvt_pk_bf16_f32 v130, v130, v34
	v_cvt_pk_bf16_f32 v131, v37, v39
	v_cvt_pk_bf16_f32 v132, v30, v33
	v_cvt_pk_bf16_f32 v133, v22, v25
	v_cvt_pk_bf16_f32 v134, v21, v18
	v_cvt_pk_bf16_f32 v135, v27, v29
	v_cvt_pk_bf16_f32 v136, v14, v10
	v_cvt_pk_bf16_f32 v137, v6, v12
	v_cvt_pk_bf16_f32 v138, v36, v35
	v_cvt_pk_bf16_f32 v139, v38, v32
	v_cvt_pk_bf16_f32 v140, v31, v24
	v_cvt_pk_bf16_f32 v141, v23, v20
	v_cvt_pk_bf16_f32 v142, v26, v19
	v_cvt_pk_bf16_f32 v143, v28, v16
	v_cvt_pk_bf16_f32 v144, v15, v11
	v_cvt_pk_bf16_f32 v145, v7, v2
	v_mul_hi_i32 v2, v172, s70
	v_lshrrev_b32_e32 v3, 31, v2
	v_ashrrev_i32_e32 v2, 2, v2
	v_add_u32_e32 v2, v2, v3
	v_mul_lo_u32 v3, v2, 24
	v_sub_u32_e32 v3, v172, v3
	v_lshrrev_b32_e32 v16, 1, v2
	v_bitop3_b32 v3, v16, v3, 7 bitop3:0x6c
	v_mul_lo_u32 v2, v2, s68
	v_lshl_add_u32 v2, v3, 4, v2
	v_add_u32_e32 v3, 0x200, v172
	v_mul_hi_i32 v4, v3, s70
	v_lshrrev_b32_e32 v5, 31, v4
	v_ashrrev_i32_e32 v4, 2, v4
	v_add_u32_e32 v4, v4, v5
	v_mul_lo_u32 v5, v4, 24
	v_sub_u32_e32 v5, v3, v5
	v_lshrrev_b32_e32 v16, 1, v4
	v_bitop3_b32 v5, v16, v5, 7 bitop3:0x6c
	v_mul_lo_u32 v4, v4, s68
	v_lshl_add_u32 v4, v5, 4, v4
	v_add_u32_e32 v5, 0x400, v172
	v_mul_hi_i32 v6, v5, s70
	v_lshrrev_b32_e32 v7, 31, v6
	v_ashrrev_i32_e32 v6, 2, v6
	v_add_u32_e32 v6, v6, v7
	v_mul_lo_u32 v7, v6, 24
	v_sub_u32_e32 v5, v5, v7
	v_lshrrev_b32_e32 v16, 1, v6
	v_bitop3_b32 v5, v16, v5, 7 bitop3:0x6c
	v_mul_lo_u32 v6, v6, s68
	v_ashrrev_i32_e32 v9, 4, v172
	v_lshl_add_u32 v6, v5, 4, v6
	v_bfe_u32 v5, v172, 2, 2
	v_lshrrev_b32_e32 v7, 1, v172
	v_and_b32_e32 v10, 0x1ffff0, v9
	v_lshrrev_b32_e32 v9, 1, v9
	v_ashrrev_i32_e32 v3, 4, v3
	v_and_or_b32 v5, v7, 8, v5
	v_and_b32_e32 v7, 0x60, v172
	v_lshlrev_b32_e32 v8, 3, v172
	v_and_b32_e32 v9, 4, v9
	v_and_b32_e32 v11, 0x1ffff0, v3
	v_lshrrev_b32_e32 v3, 1, v3
	v_and_or_b32 v7, v8, 24, v7
	v_or3_b32 v9, v10, v9, v5
	v_and_b32_e32 v3, 4, v3
	s_barrier
	global_load_lds_dwordx4 v2, s[44:45]
	s_mov_b32 m0, s72
	v_lshlrev_b32_e32 v7, 1, v7
	v_lshlrev_b32_e32 v10, 11, v9
	v_or3_b32 v3, v11, v3, v5
	global_load_lds_dwordx4 v4, s[44:45]
	s_mov_b32 m0, s73
	v_or_b32_e32 v9, v10, v7
	v_lshlrev_b32_e32 v11, 11, v3
	global_load_lds_dwordx4 v6, s[44:45]
	s_mov_b32 m0, s64
	v_or_b32_e32 v3, v11, v7
	global_load_lds_dwordx4 v9, s[46:47]
	s_mov_b32 m0, s74
	v_lshlrev_b32_e32 v13, 1, v172
	global_load_lds_dwordx4 v3, s[46:47]
	v_lshlrev_b32_e32 v9, 4, v172
	v_and_b32_e32 v14, 32, v13
	v_or_b32_e32 v3, 32, v148
	v_mul_u32_u24_e32 v5, 0x180, v168
	v_and_b32_e32 v7, 0x70, v8
	v_and_b32_e32 v12, 0xc0, v9
	v_and_or_b32 v8, v8, s75, v14
	v_and_b32_e32 v167, 63, v172
	v_bitop3_b32 v169, v3, v5, v7 bitop3:0xde
	v_or_b32_e32 v3, 64, v148
	v_add3_u32 v172, v12, 0, v8
	v_and_b32_e32 v12, 0xc0, v13
	v_and_b32_e32 v13, 48, v9
	v_bitop3_b32 v170, v3, v5, v7 bitop3:0xde
	v_or_b32_e32 v3, 0x60, v148
	v_or3_b32 v8, v11, v12, v13
	v_mov_b32_e32 v9, v149
	v_bitop3_b32 v161, v148, v5, v7 bitop3:0xde
	v_bitop3_b32 v171, v3, v5, v7 bitop3:0xde
	v_mov_b32_e32 v3, v149
	v_mov_b32_e32 v5, v149
	v_mov_b32_e32 v7, v149
	v_mul_i32_i24_e32 v15, -4, v173
	v_lshl_add_u64 v[150:151], s[48:49], 0, v[8:9]
	v_or3_b32 v8, v10, v12, v13
	v_mov_b32_e32 v16, v149
	v_mov_b32_e32 v17, v149
	v_lshl_add_u32 v160, v168, 2, s65
	v_lshl_add_u64 v[152:153], s[48:49], 0, v[8:9]
	v_lshl_add_u64 v[154:155], s[50:51], 0, v[6:7]
	v_lshl_add_u64 v[156:157], s[50:51], 0, v[4:5]
	v_lshl_add_u64 v[158:159], s[50:51], 0, v[2:3]
	v_add3_u32 v168, s63, v15, v168
	v_mov_b32_e32 v2, v149
	v_mov_b32_e32 v4, v149
	v_mov_b32_e32 v6, v149
	v_mov_b32_e32 v8, v149
	v_mov_b32_e32 v10, v149
	v_mov_b32_e32 v11, v149
	v_mov_b32_e32 v12, v149
	v_mov_b32_e32 v13, v149
	v_mov_b32_e32 v14, v149
	v_mov_b32_e32 v15, v149
	v_mov_b64_e32 v[32:33], v[16:17]
	v_mov_b64_e32 v[48:49], v[16:17]
	v_mov_b64_e32 v[64:65], v[16:17]
	v_cmp_gt_u32_e64 s[0:1], 32, v167
	v_mov_b32_e32 v173, 0
	v_mov_b32_e32 v206, 0
	v_mov_b32_e32 v207, 0
	v_mov_b32_e32 v208, 0
	v_mov_b32_e32 v209, 0
	v_mov_b32_e32 v210, 0
	v_mov_b32_e32 v211, 0
	v_mov_b32_e32 v212, 0
	v_mov_b32_e32 v213, 0
	v_mov_b32_e32 v214, 0
	v_mov_b32_e32 v215, 0
	v_mov_b32_e32 v216, 0
	v_mov_b32_e32 v217, 0
	v_mov_b32_e32 v218, 0
	v_mov_b32_e32 v219, 0
	v_mov_b32_e32 v220, 0
	v_mov_b32_e32 v221, 0
	v_mov_b64_e32 v[30:31], v[14:15]
	v_mov_b64_e32 v[28:29], v[12:13]
	v_mov_b64_e32 v[26:27], v[10:11]
	v_mov_b64_e32 v[24:25], v[8:9]
	v_mov_b64_e32 v[22:23], v[6:7]
	v_mov_b64_e32 v[20:21], v[4:5]
	v_mov_b64_e32 v[18:19], v[2:3]
	v_mov_b64_e32 v[46:47], v[14:15]
	v_mov_b64_e32 v[44:45], v[12:13]
	v_mov_b64_e32 v[42:43], v[10:11]
	v_mov_b64_e32 v[40:41], v[8:9]
	v_mov_b64_e32 v[38:39], v[6:7]
	v_mov_b64_e32 v[36:37], v[4:5]
	v_mov_b64_e32 v[34:35], v[2:3]
	v_mov_b64_e32 v[62:63], v[14:15]
	v_mov_b64_e32 v[60:61], v[12:13]
	v_mov_b64_e32 v[58:59], v[10:11]
	v_mov_b64_e32 v[56:57], v[8:9]
	v_mov_b64_e32 v[54:55], v[6:7]
	v_mov_b64_e32 v[52:53], v[4:5]
	v_mov_b64_e32 v[50:51], v[2:3]
	v_mov_b32_e32 v174, 0

.LBB0_807:
	s_mul_i32 s56, s87, 0x6000
	s_add_i32 s56, s56, 0
	s_add_i32 s56, s56, 0x8000
	v_add_u32_e32 v175, s56, v161
	ds_read_b128 v[66:69], v175 offset:0
	ds_read_b128 v[70:73], v175 offset:0x3000
	v_add_u32_e32 v200, s56, v169
	ds_read_b128 v[176:179], v200 offset:0
	ds_read_b128 v[180:183], v200 offset:0x3000
	v_add_u32_e32 v201, s56, v170
	ds_read_b128 v[184:187], v201 offset:0
	ds_read_b128 v[188:191], v201 offset:0x3000
	s_waitcnt lgkmcnt(4)
	v_add_u32_e32 v202, s56, v171
	v_mfma_f32_32x32x16_bf16 v[82:97], v[66:69], v[98:101], v[206:221]
	ds_read_b128 v[192:195], v202 offset:0
	ds_read_b128 v[196:199], v202 offset:0x3000
	s_waitcnt lgkmcnt(4)
	v_mfma_f32_32x32x16_bf16 v[66:81], v[70:73], v[98:101], v[206:221]
	v_mfma_f32_32x32x16_bf16 v[82:97], v[176:179], v[102:105], v[82:97]
	ds_read_b128 v[176:179], v175 offset:0x80
	v_mfma_f32_32x32x16_bf16 v[66:81], v[180:183], v[102:105], v[66:81]
	ds_read_b128 v[180:183], v175 offset:0x3080
	s_waitcnt lgkmcnt(4)
	v_mfma_f32_32x32x16_bf16 v[82:97], v[184:187], v[106:109], v[82:97]
	ds_read_b128 v[184:187], v200 offset:0x80
	v_mfma_f32_32x32x16_bf16 v[66:81], v[188:191], v[106:109], v[66:81]
	ds_read_b128 v[188:191], v200 offset:0x3080
	s_waitcnt lgkmcnt(4)
	v_mfma_f32_32x32x16_bf16 v[82:97], v[192:195], v[110:113], v[82:97]
	ds_read_b128 v[192:195], v201 offset:0x80
	v_mfma_f32_32x32x16_bf16 v[66:81], v[196:199], v[110:113], v[66:81]
	ds_read_b128 v[196:199], v201 offset:0x3080
	s_waitcnt lgkmcnt(4)
	v_mfma_f32_32x32x16_bf16 v[82:97], v[176:179], v[114:117], v[82:97]
	ds_read_b128 v[176:179], v202 offset:0x80
	v_mfma_f32_32x32x16_bf16 v[66:81], v[180:183], v[114:117], v[66:81]
	ds_read_b128 v[180:183], v202 offset:0x3080
	s_waitcnt lgkmcnt(4)
	v_mfma_f32_32x32x16_bf16 v[82:97], v[184:187], v[118:121], v[82:97]
	ds_read_b128 v[184:187], v175 offset:0x100
	v_mfma_f32_32x32x16_bf16 v[66:81], v[188:191], v[118:121], v[66:81]
	ds_read_b128 v[188:191], v175 offset:0x3100
	s_waitcnt lgkmcnt(4)
	v_mfma_f32_32x32x16_bf16 v[82:97], v[192:195], v[122:125], v[82:97]
	ds_read_b128 v[192:195], v200 offset:0x100
	v_mfma_f32_32x32x16_bf16 v[66:81], v[196:199], v[122:125], v[66:81]
	ds_read_b128 v[196:199], v200 offset:0x3100
	s_waitcnt lgkmcnt(4)
	v_mfma_f32_32x32x16_bf16 v[82:97], v[176:179], v[126:129], v[82:97]
	ds_read_b128 v[176:179], v201 offset:0x100
	v_mfma_f32_32x32x16_bf16 v[66:81], v[180:183], v[126:129], v[66:81]
	ds_read_b128 v[180:183], v201 offset:0x3100
	s_waitcnt lgkmcnt(4)
	v_mfma_f32_32x32x16_bf16 v[82:97], v[184:187], v[130:133], v[82:97]
	ds_read_b128 v[184:187], v202 offset:0x100
	v_mfma_f32_32x32x16_bf16 v[66:81], v[188:191], v[130:133], v[66:81]
	ds_read_b128 v[188:191], v202 offset:0x3100
	s_waitcnt lgkmcnt(4)
	v_mfma_f32_32x32x16_bf16 v[82:97], v[192:195], v[134:137], v[82:97]
	s_waitcnt lgkmcnt(2)
	v_mfma_f32_32x32x16_bf16 v[66:81], v[196:199], v[134:137], v[66:81]
	v_mfma_f32_32x32x16_bf16 v[82:97], v[176:179], v[138:141], v[82:97]
	s_waitcnt lgkmcnt(0)
	v_mfma_f32_32x32x16_bf16 v[66:81], v[180:183], v[138:141], v[66:81]
	v_mfma_f32_32x32x16_bf16 v[82:97], v[184:187], v[142:145], v[82:97]
	s_add_i32 s56, s86, 0x13f
	s_cmp_le_i32 s56, s84
	v_mfma_f32_32x32x16_bf16 v[66:81], v[188:191], v[142:145], v[66:81]
	s_cbranch_scc1 .LBB0_809
	v_add_u32_e32 v175, s83, v168
	v_cmp_lt_i32_e32 vcc, -1, v175
	v_add_u32_e32 v176, -1, v175
	s_nop 4
	v_cndmask_b32_e32 v82, v165, v82, vcc
	v_cmp_lt_i32_e32 vcc, 31, v175
	s_nop 1
	v_cndmask_b32_e32 v66, v165, v66, vcc
	v_cmp_lt_i32_e32 vcc, -1, v176
	s_nop 1
	v_cndmask_b32_e32 v83, v165, v83, vcc
	v_cmp_lt_i32_e32 vcc, 31, v176
	v_add_u32_e32 v176, -2, v175
	s_nop 0
	v_cndmask_b32_e32 v67, v165, v67, vcc
	v_cmp_lt_i32_e32 vcc, -1, v176
	s_nop 1
	v_cndmask_b32_e32 v84, v165, v84, vcc
	v_cmp_lt_i32_e32 vcc, 31, v176
	v_add_u32_e32 v176, -3, v175
	s_nop 0
	v_cndmask_b32_e32 v68, v165, v68, vcc
	v_cmp_lt_i32_e32 vcc, -1, v176
	s_nop 1
	v_cndmask_b32_e32 v85, v165, v85, vcc
	v_cmp_lt_i32_e32 vcc, 31, v176
	v_add_u32_e32 v176, -8, v175
	s_nop 0
	v_cndmask_b32_e32 v69, v165, v69, vcc
	v_cmp_lt_i32_e32 vcc, -1, v176
	s_nop 1
	v_cndmask_b32_e32 v86, v165, v86, vcc
	v_cmp_lt_i32_e32 vcc, 31, v176
	v_add_u32_e32 v176, -9, v175
	s_nop 0
	v_cndmask_b32_e32 v70, v165, v70, vcc
	v_cmp_lt_i32_e32 vcc, -1, v176
	s_nop 1
	v_cndmask_b32_e32 v87, v165, v87, vcc
	v_cmp_lt_i32_e32 vcc, 31, v176
	v_add_u32_e32 v176, -10, v175
	s_nop 0
	v_cndmask_b32_e32 v71, v165, v71, vcc
	v_cmp_lt_i32_e32 vcc, -1, v176
	s_nop 1
	v_cndmask_b32_e32 v88, v165, v88, vcc
	v_cmp_lt_i32_e32 vcc, 31, v176
	v_add_u32_e32 v176, -11, v175
	s_nop 0
	v_cndmask_b32_e32 v72, v165, v72, vcc
	v_cmp_lt_i32_e32 vcc, -1, v176
	s_nop 1
	v_cndmask_b32_e32 v89, v165, v89, vcc
	v_cmp_lt_i32_e32 vcc, 31, v176
	v_add_u32_e32 v176, -16, v175
	s_nop 0
	v_cndmask_b32_e32 v73, v165, v73, vcc
	v_cmp_lt_i32_e32 vcc, -1, v176
	s_nop 1
	v_cndmask_b32_e32 v90, v165, v90, vcc
	v_cmp_lt_i32_e32 vcc, 31, v176
	v_subrev_u32_e32 v176, 17, v175
	s_nop 0
	v_cndmask_b32_e32 v74, v165, v74, vcc
	v_cmp_lt_i32_e32 vcc, -1, v176
	s_nop 1
	v_cndmask_b32_e32 v91, v165, v91, vcc
	v_cmp_lt_i32_e32 vcc, 31, v176
	v_subrev_u32_e32 v176, 18, v175
	s_nop 0
	v_cndmask_b32_e32 v75, v165, v75, vcc
	v_cmp_lt_i32_e32 vcc, -1, v176
	s_nop 1
	v_cndmask_b32_e32 v92, v165, v92, vcc
	v_cmp_lt_i32_e32 vcc, 31, v176
	v_subrev_u32_e32 v176, 19, v175
	s_nop 0
	v_cndmask_b32_e32 v76, v165, v76, vcc
	v_cmp_lt_i32_e32 vcc, -1, v176
	s_nop 1
	v_cndmask_b32_e32 v93, v165, v93, vcc
	v_cmp_lt_i32_e32 vcc, 31, v176
	v_subrev_u32_e32 v176, 24, v175
	s_nop 0
	v_cndmask_b32_e32 v77, v165, v77, vcc
	v_cmp_lt_i32_e32 vcc, -1, v176
	s_nop 1
	v_cndmask_b32_e32 v94, v165, v94, vcc
	v_cmp_lt_i32_e32 vcc, 31, v176
	v_subrev_u32_e32 v176, 25, v175
	s_nop 0
	v_cndmask_b32_e32 v78, v165, v78, vcc
	v_cmp_lt_i32_e32 vcc, -1, v176
	s_nop 1
	v_cndmask_b32_e32 v95, v165, v95, vcc
	v_cmp_lt_i32_e32 vcc, 31, v176
	v_subrev_u32_e32 v176, 26, v175
	v_subrev_u32_e32 v175, 27, v175
	v_cndmask_b32_e32 v79, v165, v79, vcc
	v_cmp_lt_i32_e32 vcc, -1, v176
	s_nop 1
	v_cndmask_b32_e32 v96, v165, v96, vcc
	v_cmp_lt_i32_e32 vcc, 31, v176
	s_nop 1
	v_cndmask_b32_e32 v80, v165, v80, vcc
	v_cmp_lt_i32_e32 vcc, -1, v175
	s_nop 1
	v_cndmask_b32_e32 v97, v165, v97, vcc
	v_cmp_lt_i32_e32 vcc, 31, v175
	s_nop 1
	v_cndmask_b32_e32 v81, v165, v81, vcc
.LBB0_809:
	s_nop 7
	v_max_f32_e32 v175, v83, v83
	v_max_f32_e32 v176, v82, v82
	v_max_f32_e32 v175, v176, v175
	v_max3_f32 v175, v175, v84, v85
	v_max3_f32 v175, v175, v86, v87
	v_max3_f32 v175, v175, v88, v89
	v_max3_f32 v175, v175, v90, v91
	v_max3_f32 v175, v175, v92, v93
	v_max3_f32 v175, v175, v94, v95
	v_max3_f32 v175, v175, v96, v97
	v_max3_f32 v175, v175, v66, v67
	v_max3_f32 v175, v175, v68, v69
	v_max3_f32 v175, v175, v70, v71
	v_max3_f32 v175, v175, v72, v73
	v_max3_f32 v175, v175, v74, v75
	v_max3_f32 v175, v175, v76, v77
	v_max3_f32 v175, v175, v78, v79
	v_max3_f32 v175, v175, v80, v81
	v_mov_b32_e32 v176, v175
	s_nop 1
	v_permlane32_swap_b32_e32 v175, v176
	v_max_f32_e32 v176, v176, v176
	v_max_f32_e32 v175, v175, v175
	v_max_f32_e32 v175, v175, v176
	v_cmp_ge_f32_e32 vcc, s76, v175
	s_cmp_eq_u64 vcc, exec
	s_cbranch_scc0 .Lsm1_slow
	v_mov_b32_e32 v222, 1.0
.Lsm1_join:
	v_exp_f32_e32 v82, v82
	v_exp_f32_e32 v66, v66
	v_exp_f32_e32 v175, v83
	v_exp_f32_e32 v67, v67
	v_exp_f32_e32 v84, v84
	v_exp_f32_e32 v68, v68
	v_exp_f32_e32 v85, v85
	v_exp_f32_e32 v69, v69
	v_add_f32_e32 v83, v66, v82
	v_exp_f32_e32 v86, v86
	v_exp_f32_e32 v70, v70
	v_add_f32_e32 v83, 0, v83
	v_add_f32_e32 v176, v67, v175
	v_add_f32_e32 v83, v176, v83
	v_add_f32_e32 v176, v68, v84
	v_add_f32_e32 v83, v176, v83
	v_add_f32_e32 v176, v69, v85
	v_add_f32_e32 v83, v176, v83
	v_add_f32_e32 v176, v70, v86
	v_exp_f32_e32 v87, v87
	v_exp_f32_e32 v71, v71
	v_add_f32_e32 v178, v176, v83
	v_exp_f32_e32 v88, v88
	v_exp_f32_e32 v72, v72
	v_add_f32_e32 v179, v71, v87
	v_exp_f32_e32 v176, v89
	v_exp_f32_e32 v83, v73
	v_add_f32_e32 v73, v179, v178
	v_add_f32_e32 v89, v72, v88
	v_add_f32_e32 v178, v89, v73
	v_exp_f32_e32 v89, v90
	v_exp_f32_e32 v73, v74
	v_add_f32_e32 v179, v83, v176
	v_exp_f32_e32 v90, v91
	v_mov_b32_e32 v74, v75
	v_add_f32_e32 v75, v179, v178
	v_add_f32_e32 v91, v73, v89
	v_add_f32_e32 v178, v91, v75
	v_exp_f32_e32 v74, v74
	v_exp_f32_e32 v91, v92
	v_exp_f32_e32 v75, v76
	v_add_f32_e32 v179, v74, v90
	v_exp_f32_e32 v92, v93
	v_mov_b32_e32 v76, v77
	v_add_f32_e32 v77, v179, v178
	v_add_f32_e32 v93, v75, v91
	v_add_f32_e32 v178, v93, v77
	v_exp_f32_e32 v76, v76
	v_exp_f32_e32 v93, v94
	v_exp_f32_e32 v77, v78
	v_add_f32_e32 v179, v76, v92
	v_exp_f32_e32 v94, v95
	v_mov_b32_e32 v78, v79
	v_add_f32_e32 v79, v179, v178
	v_add_f32_e32 v95, v77, v93
	v_exp_f32_e32 v78, v78
	v_add_f32_e32 v79, v95, v79
	v_exp_f32_e32 v95, v96
	v_exp_f32_e32 v80, v80
	v_exp_f32_e32 v96, v97
	v_exp_f32_e32 v81, v81
	v_add_f32_e32 v178, v78, v94
	v_add_f32_e32 v79, v178, v79
	v_add_f32_e32 v97, v80, v95
	v_add_f32_e32 v79, v97, v79
	v_add_f32_e32 v97, v81, v96
	v_add_f32_e32 v79, v97, v79
	v_mov_b32_e32 v97, v222
	v_mov_b32_e32 v177, v79
	s_nop 1
	v_permlane32_swap_b32_e32 v79, v177
	v_cmp_gt_f32_e32 vcc, 1.0, v97


	s_cbranch_vccz .LBB0_813
	s_and_saveexec_b64 s[56:57], s[0:1]
	ds_write_b32 v160, v97
	s_or_b64 exec, exec, s[56:57]
	s_waitcnt lgkmcnt(0)
	v_add_u32_e32 v190, s65, v148
	ds_read_b128 v[178:181], v190 offset:96
	ds_read_b128 v[182:185], v190 offset:64
	ds_read_b128 v[186:189], v190 offset:32
	ds_read_b128 v[190:193], v190
	s_waitcnt lgkmcnt(0)
	v_pk_mul_f32 v[62:63], v[62:63], v[178:179]
	v_pk_mul_f32 v[58:59], v[58:59], v[182:183]
	v_pk_mul_f32 v[54:55], v[54:55], v[186:187]
	v_pk_mul_f32 v[64:65], v[64:65], v[180:181]
	v_pk_mul_f32 v[60:61], v[60:61], v[184:185]
	v_pk_mul_f32 v[56:57], v[56:57], v[188:189]
	v_pk_mul_f32 v[52:53], v[52:53], v[192:193]
	v_pk_mul_f32 v[50:51], v[50:51], v[190:191]
	v_pk_mul_f32 v[46:47], v[46:47], v[178:179]
	v_pk_mul_f32 v[42:43], v[42:43], v[182:183]
	v_pk_mul_f32 v[38:39], v[38:39], v[186:187]
	v_pk_mul_f32 v[48:49], v[48:49], v[180:181]
	v_pk_mul_f32 v[44:45], v[44:45], v[184:185]
	v_pk_mul_f32 v[40:41], v[40:41], v[188:189]
	v_pk_mul_f32 v[36:37], v[36:37], v[192:193]
	v_pk_mul_f32 v[34:35], v[34:35], v[190:191]
	v_pk_mul_f32 v[30:31], v[30:31], v[178:179]
	v_pk_mul_f32 v[26:27], v[26:27], v[182:183]
	v_pk_mul_f32 v[22:23], v[22:23], v[186:187]
	v_pk_mul_f32 v[32:33], v[32:33], v[180:181]
	v_pk_mul_f32 v[28:29], v[28:29], v[184:185]
	v_pk_mul_f32 v[24:25], v[24:25], v[188:189]
	v_pk_mul_f32 v[20:21], v[20:21], v[192:193]
	v_pk_mul_f32 v[18:19], v[18:19], v[190:191]
	v_pk_mul_f32 v[14:15], v[14:15], v[178:179]
	v_pk_mul_f32 v[10:11], v[10:11], v[182:183]
	v_pk_mul_f32 v[6:7], v[6:7], v[186:187]
	v_pk_mul_f32 v[16:17], v[16:17], v[180:181]
	v_pk_mul_f32 v[12:13], v[12:13], v[184:185]
	v_pk_mul_f32 v[8:9], v[8:9], v[188:189]
	v_pk_mul_f32 v[4:5], v[4:5], v[192:193]
	v_pk_mul_f32 v[2:3], v[2:3], v[190:191]

.Lsm1_slow:
	v_max_f32_e32 v175, 0, v175
	v_sub_f32_e32 v66, v66, v175
	v_sub_f32_e32 v67, v67, v175
	v_sub_f32_e32 v68, v68, v175
	v_sub_f32_e32 v69, v69, v175
	v_sub_f32_e32 v70, v70, v175
	v_sub_f32_e32 v71, v71, v175
	v_sub_f32_e32 v72, v72, v175
	v_sub_f32_e32 v73, v73, v175
	v_sub_f32_e32 v74, v74, v175
	v_sub_f32_e32 v75, v75, v175
	v_sub_f32_e32 v76, v76, v175
	v_sub_f32_e32 v77, v77, v175
	v_sub_f32_e32 v78, v78, v175
	v_sub_f32_e32 v79, v79, v175
	v_sub_f32_e32 v80, v80, v175
	v_sub_f32_e32 v81, v81, v175
	v_sub_f32_e32 v82, v82, v175
	v_sub_f32_e32 v83, v83, v175
	v_sub_f32_e32 v84, v84, v175
	v_sub_f32_e32 v85, v85, v175
	v_sub_f32_e32 v86, v86, v175
	v_sub_f32_e32 v87, v87, v175
	v_sub_f32_e32 v88, v88, v175
	v_sub_f32_e32 v89, v89, v175
	v_sub_f32_e32 v90, v90, v175
	v_sub_f32_e32 v91, v91, v175
	v_sub_f32_e32 v92, v92, v175
	v_sub_f32_e32 v93, v93, v175
	v_sub_f32_e32 v94, v94, v175
	v_sub_f32_e32 v95, v95, v175
	v_sub_f32_e32 v96, v96, v175
	v_sub_f32_e32 v97, v97, v175
	v_exp_f32_e64 v222, -v175
	v_add_f32_e32 v173, v173, v175
	v_sub_f32_e32 v206, 0, v173
	v_mov_b32_e32 v207, v206
	v_mov_b32_e32 v208, v206
	v_mov_b32_e32 v209, v206
	v_mov_b32_e32 v210, v206
	v_mov_b32_e32 v211, v206
	v_mov_b32_e32 v212, v206
	v_mov_b32_e32 v213, v206
	v_mov_b32_e32 v214, v206
	v_mov_b32_e32 v215, v206
	v_mov_b32_e32 v216, v206
	v_mov_b32_e32 v217, v206
	v_mov_b32_e32 v218, v206
	v_mov_b32_e32 v219, v206
	v_mov_b32_e32 v220, v206
	v_mov_b32_e32 v221, v206
	s_branch .Lsm1_join

.LBB0_945:
	s_or_b64 exec, exec, s[0:1]
	s_lshl_b32 s55, s80, 8
	s_and_b32 s0, s81, 15
	s_add_i32 s55, s55, s63
	s_lshl_b32 s54, s0, 8
	v_mov_b32_e32 v168, v1
	s_ashr_i32 s0, s55, 31
	s_add_u32 s52, s52, s55
	v_and_b32_e32 v167, 31, v168
	v_or_b32_e32 v30, s52, v167
	v_mov_b64_e32 v[2:3], s[6:7]
	s_addc_u32 s53, s53, s0
	v_mad_u64_u32 v[2:3], s[0:1], v30, s68, v[2:3]
	v_bfe_u32 v169, v168, 5, 1
	v_mad_i32_i24 v3, s53, v162, v3
	s_lshl_b32 s12, s82, 1
	v_lshl_add_u64 v[2:3], v[2:3], 0, s[12:13]
	v_lshlrev_b32_e32 v148, 4, v169
	v_lshl_add_u64 v[44:45], v[2:3], 0, v[148:149]
	global_load_dwordx4 v[32:35], v[44:45], off
	global_load_dwordx4 v[36:39], v[44:45], off offset:32
	global_load_dwordx4 v[26:29], v[44:45], off offset:64
	global_load_dwordx4 v[22:25], v[44:45], off offset:96
	global_load_dwordx4 v[18:21], v[44:45], off offset:128
	global_load_dwordx4 v[14:17], v[44:45], off offset:160
	global_load_dwordx4 v[10:13], v[44:45], off offset:192
	v_and_b32_e32 v118, 32, v168
	global_load_dwordx4 v[6:9], v118, s[4:5] offset:576
	s_waitcnt lgkmcnt(0)
	global_load_dwordx4 v[2:5], v118, s[4:5] offset:592
	global_load_dwordx4 v[102:105], v118, s[4:5] offset:704
	global_load_dwordx4 v[110:113], v118, s[4:5] offset:720
	global_load_dwordx4 v[40:43], v[44:45], off offset:224
	global_load_dwordx4 v[82:85], v[44:45], off offset:256
	global_load_dwordx4 v[138:141], v[44:45], off offset:288
	global_load_dwordx4 v[70:73], v[44:45], off offset:320
	global_load_dwordx4 v[142:145], v[44:45], off offset:352
	v_mov_b32_e32 v31, s53
	s_mov_b32 m0, s71
	s_mov_b32 s12, 1
	s_waitcnt vmcnt(0)
	v_and_b32_e32 v191, 0xffff0000, v32
	v_lshlrev_b32_e32 v190, 16, v32
	v_lshlrev_b32_e32 v206, 16, v26
	v_and_b32_e32 v207, 0xffff0000, v26
	v_lshlrev_b32_e32 v208, 16, v27
	v_and_b32_e32 v209, 0xffff0000, v27
	v_lshlrev_b32_e32 v210, 16, v28
	v_and_b32_e32 v211, 0xffff0000, v28
	v_lshlrev_b32_e32 v212, 16, v29
	v_and_b32_e32 v213, 0xffff0000, v29
	v_lshlrev_b32_e32 v222, 16, v18
	v_and_b32_e32 v223, 0xffff0000, v18
	v_lshlrev_b32_e32 v224, 16, v19
	v_and_b32_e32 v225, 0xffff0000, v19
	v_lshlrev_b32_e32 v226, 16, v20
	v_and_b32_e32 v227, 0xffff0000, v20
	v_lshlrev_b32_e32 v228, 16, v21
	v_and_b32_e32 v229, 0xffff0000, v21
	global_load_dwordx4 v[26:29], v118, s[4:5] offset:640
	global_load_dwordx4 v[156:159], v118, s[4:5] offset:656
	global_load_dwordx4 v[18:21], v118, s[4:5] offset:528
	v_mul_f32_e32 v188, v191, v191
	v_lshlrev_b32_e32 v192, 16, v33
	v_fmac_f32_e32 v188, v190, v190
	v_and_b32_e32 v193, 0xffff0000, v33
	v_fmac_f32_e32 v188, v192, v192
	v_lshlrev_b32_e32 v194, 16, v34
	v_fmac_f32_e32 v188, v193, v193
	v_and_b32_e32 v195, 0xffff0000, v34
	v_fmac_f32_e32 v188, v194, v194
	v_lshlrev_b32_e32 v196, 16, v35
	v_fmac_f32_e32 v188, v195, v195
	v_and_b32_e32 v197, 0xffff0000, v35
	v_fmac_f32_e32 v188, v196, v196
	v_lshlrev_b32_e32 v198, 16, v36
	v_fmac_f32_e32 v188, v197, v197
	v_and_b32_e32 v199, 0xffff0000, v36
	v_fmac_f32_e32 v188, v198, v198
	v_lshlrev_b32_e32 v200, 16, v37
	v_lshlrev_b32_e32 v214, 16, v22
	v_and_b32_e32 v215, 0xffff0000, v22
	v_lshlrev_b32_e32 v216, 16, v23
	v_and_b32_e32 v217, 0xffff0000, v23
	v_lshlrev_b32_e32 v218, 16, v24
	v_and_b32_e32 v219, 0xffff0000, v24
	v_lshlrev_b32_e32 v220, 16, v25
	v_and_b32_e32 v221, 0xffff0000, v25
	v_fmac_f32_e32 v188, v199, v199
	global_load_dwordx4 v[22:25], v118, s[4:5] offset:512
	v_and_b32_e32 v201, 0xffff0000, v37
	v_fmac_f32_e32 v188, v200, v200
	v_lshlrev_b32_e32 v202, 16, v38
	v_fmac_f32_e32 v188, v201, v201
	v_and_b32_e32 v203, 0xffff0000, v38
	v_fmac_f32_e32 v188, v202, v202
	v_lshlrev_b32_e32 v204, 16, v39
	v_fmac_f32_e32 v188, v203, v203
	v_and_b32_e32 v205, 0xffff0000, v39
	v_fmac_f32_e32 v188, v204, v204
	v_fmac_f32_e32 v188, v205, v205
	v_fmac_f32_e32 v188, v206, v206
	v_fmac_f32_e32 v188, v207, v207
	v_fmac_f32_e32 v188, v208, v208
	v_fmac_f32_e32 v188, v209, v209
	v_fmac_f32_e32 v188, v210, v210
	v_fmac_f32_e32 v188, v211, v211
	v_fmac_f32_e32 v188, v212, v212
	v_fmac_f32_e32 v188, v213, v213
	v_fmac_f32_e32 v188, v214, v214
	v_fmac_f32_e32 v188, v215, v215
	v_fmac_f32_e32 v188, v216, v216
	v_fmac_f32_e32 v188, v217, v217
	v_fmac_f32_e32 v188, v218, v218
	v_fmac_f32_e32 v188, v219, v219
	v_fmac_f32_e32 v188, v220, v220
	v_fmac_f32_e32 v188, v221, v221
	v_fmac_f32_e32 v188, v222, v222
	v_fmac_f32_e32 v188, v223, v223
	v_fmac_f32_e32 v188, v224, v224
	v_fmac_f32_e32 v188, v225, v225
	v_fmac_f32_e32 v188, v226, v226
	v_fmac_f32_e32 v188, v227, v227
	v_fmac_f32_e32 v188, v228, v228
	v_lshlrev_b32_e32 v230, 16, v14
	v_fmac_f32_e32 v188, v229, v229
	v_and_b32_e32 v231, 0xffff0000, v14
	v_fmac_f32_e32 v188, v230, v230
	v_lshlrev_b32_e32 v232, 16, v15
	v_fmac_f32_e32 v188, v231, v231
	v_and_b32_e32 v233, 0xffff0000, v15
	v_fmac_f32_e32 v188, v232, v232
	v_lshlrev_b32_e32 v234, 16, v16
	v_fmac_f32_e32 v188, v233, v233
	v_and_b32_e32 v235, 0xffff0000, v16
	v_fmac_f32_e32 v188, v234, v234
	v_lshlrev_b32_e32 v246, 16, v40
	v_and_b32_e32 v247, 0xffff0000, v40
	v_lshlrev_b32_e32 v248, 16, v41
	v_and_b32_e32 v249, 0xffff0000, v41
	v_lshlrev_b32_e32 v250, 16, v42
	v_and_b32_e32 v251, 0xffff0000, v42
	v_lshlrev_b32_e32 v252, 16, v43
	v_and_b32_e32 v253, 0xffff0000, v43
	global_load_dwordx4 v[106:109], v118, s[4:5] offset:16
	global_load_dwordx4 v[114:117], v118, s[4:5]
	global_load_dwordx4 v[94:97], v118, s[4:5] offset:80
	global_load_dwordx4 v[98:101], v118, s[4:5] offset:64
	global_load_dwordx4 v[86:89], v118, s[4:5] offset:144
	global_load_dwordx4 v[90:93], v118, s[4:5] offset:128
	global_load_dwordx4 v[74:77], v118, s[4:5] offset:208
	global_load_dwordx4 v[78:81], v118, s[4:5] offset:192
	global_load_dwordx4 v[62:65], v118, s[4:5] offset:272
	global_load_dwordx4 v[66:69], v118, s[4:5] offset:256
	global_load_dwordx4 v[54:57], v118, s[4:5] offset:336
	global_load_dwordx4 v[58:61], v118, s[4:5] offset:320
	global_load_dwordx4 v[46:49], v118, s[4:5] offset:400
	global_load_dwordx4 v[50:53], v118, s[4:5] offset:384
	global_load_dwordx4 v[38:41], v118, s[4:5] offset:464
	global_load_dwordx4 v[42:45], v118, s[4:5] offset:448
	v_lshlrev_b32_e32 v236, 16, v17
	v_fmac_f32_e32 v188, v235, v235
	v_and_b32_e32 v237, 0xffff0000, v17
	v_fmac_f32_e32 v188, v236, v236
	v_lshlrev_b32_e32 v238, 16, v10
	v_fmac_f32_e32 v188, v237, v237
	v_and_b32_e32 v239, 0xffff0000, v10
	v_fmac_f32_e32 v188, v238, v238
	v_lshlrev_b32_e32 v240, 16, v11
	v_fmac_f32_e32 v188, v239, v239
	v_and_b32_e32 v241, 0xffff0000, v11
	v_fmac_f32_e32 v188, v240, v240
	v_lshlrev_b32_e32 v242, 16, v12
	v_fmac_f32_e32 v188, v241, v241
	v_and_b32_e32 v243, 0xffff0000, v12
	v_fmac_f32_e32 v188, v242, v242
	v_lshlrev_b32_e32 v244, 16, v13
	v_fmac_f32_e32 v188, v243, v243
	v_and_b32_e32 v245, 0xffff0000, v13
	v_fmac_f32_e32 v188, v244, v244
	v_fmac_f32_e32 v188, v245, v245
	v_fmac_f32_e32 v188, v246, v246
	v_fmac_f32_e32 v188, v247, v247
	v_fmac_f32_e32 v188, v248, v248
	v_fmac_f32_e32 v188, v249, v249
	v_fmac_f32_e32 v188, v250, v250
	v_fmac_f32_e32 v188, v251, v251
	v_fmac_f32_e32 v188, v252, v252
	v_lshlrev_b32_e32 v187, 16, v82
	v_lshlrev_b32_e32 v186, 16, v70
	v_fmac_f32_e32 v188, v253, v253
	v_lshlrev_b32_e32 v124, 16, v144
	v_and_b32_e32 v126, 0xffff0000, v144
	v_lshlrev_b32_e32 v131, 16, v139
	v_and_b32_e32 v133, 0xffff0000, v139
	v_lshlrev_b32_e32 v137, 16, v138
	v_lshlrev_b32_e32 v136, 16, v142
	v_and_b32_e32 v139, 0xffff0000, v138
	v_and_b32_e32 v138, 0xffff0000, v142
	v_lshlrev_b32_e32 v142, 16, v73
	v_and_b32_e32 v144, 0xffff0000, v73
	v_lshlrev_b32_e32 v152, 16, v72
	v_and_b32_e32 v154, 0xffff0000, v72
	v_pk_mul_f32 v[72:73], v[186:187], v[186:187]
	s_waitcnt vmcnt(18)
	v_mov_b32_e32 v150, v158
	v_mov_b32_e32 v158, v156
	v_lshlrev_b32_e32 v156, 16, v71
	v_and_b32_e32 v184, 0xffff0000, v71
	v_and_b32_e32 v189, 0xffff0000, v82
	v_add_f32_e32 v71, v73, v188
	v_and_b32_e32 v188, 0xffff0000, v70
	v_mov_b32_e32 v128, v110
	v_mov_b32_e32 v129, v2
	v_mov_b32_e32 v2, v111
	s_waitcnt vmcnt(17)
	v_mov_b32_e32 v151, v20
	v_mov_b32_e32 v20, v159
	v_mov_b32_e32 v159, v18
	v_mov_b32_e32 v18, v157
	v_lshlrev_b32_e32 v157, 16, v83
	v_pk_mul_f32 v[110:111], v[188:189], v[188:189]
	v_lshlrev_b32_e32 v119, 16, v141
	v_and_b32_e32 v121, 0xffff0000, v141
	v_lshlrev_b32_e32 v125, 16, v140
	v_and_b32_e32 v127, 0xffff0000, v140
	v_mov_b32_e32 v140, v102
	v_mov_b32_e32 v141, v6
	v_mov_b32_e32 v6, v103
	v_pk_mul_f32 v[102:103], v[156:157], v[156:157]
	v_and_b32_e32 v185, 0xffff0000, v83
	v_add_f32_e32 v70, v111, v71
	v_mov_b32_e32 v134, v104
	v_mov_b32_e32 v135, v8
	v_mov_b32_e32 v8, v105
	v_lshlrev_b32_e32 v153, 16, v84
	v_pk_mul_f32 v[104:105], v[184:185], v[184:185]
	v_add_f32_e32 v70, v103, v70
	v_pk_mul_f32 v[180:181], v[152:153], v[152:153]
	v_and_b32_e32 v155, 0xffff0000, v84
	v_add_f32_e32 v70, v105, v70
	v_lshlrev_b32_e32 v130, 16, v143
	v_and_b32_e32 v132, 0xffff0000, v143
	v_lshlrev_b32_e32 v143, 16, v85
	v_pk_mul_f32 v[182:183], v[154:155], v[154:155]
	v_add_f32_e32 v70, v181, v70
	v_lshlrev_b32_e32 v118, 16, v145
	v_and_b32_e32 v120, 0xffff0000, v145
	v_pk_mul_f32 v[176:177], v[142:143], v[142:143]
	v_and_b32_e32 v145, 0xffff0000, v85
	v_add_f32_e32 v70, v183, v70
	v_pk_mul_f32 v[178:179], v[144:145], v[144:145]
	v_add_f32_e32 v70, v177, v70
	v_pk_mul_f32 v[172:173], v[136:137], v[136:137]
	v_add_f32_e32 v70, v179, v70
	v_pk_mul_f32 v[174:175], v[138:139], v[138:139]
	v_add_f32_e32 v70, v173, v70
	v_add_f32_e32 v70, v175, v70
	v_fmac_f32_e32 v70, v131, v131
	v_fmac_f32_e32 v70, v133, v133
	v_fmac_f32_e32 v70, v125, v125
	v_fmac_f32_e32 v70, v127, v127
	v_fmac_f32_e32 v70, v119, v119
	v_fmac_f32_e32 v70, v121, v121
	v_add_f32_e32 v103, v72, v70
	v_add_f32_e32 v103, v110, v103
	v_add_f32_e32 v102, v102, v103
	v_add_f32_e32 v173, v104, v102
	v_add_f32_e32 v173, v180, v173
	v_add_f32_e32 v173, v182, v173
	v_add_f32_e32 v173, v176, v173
	v_add_f32_e32 v173, v178, v173
	v_mov_b32_e32 v176, v132
	v_mov_b32_e32 v177, v130
	s_waitcnt vmcnt(16)
	v_mov_b32_e32 v179, v24
	v_add_f32_e32 v24, v172, v173
	v_lshlrev_b64 v[10:11], 8, v[30:31]
	v_pk_mul_f32 v[176:177], v[176:177], v[176:177]
	v_add_f32_e32 v24, v174, v24
	v_lshl_add_u64 v[10:11], s[10:11], 0, v[10:11]
	v_lshlrev_b32_e32 v12, 6, v169
	v_mov_b32_e32 v13, v149
	v_mov_b32_e32 v180, v126
	v_mov_b32_e32 v181, v124
	v_add_f32_e32 v24, v177, v24
	v_lshl_add_u64 v[170:171], v[10:11], 0, v[12:13]
	v_pk_mul_f32 v[180:181], v[180:181], v[180:181]
	v_add_f32_e32 v24, v176, v24
	global_load_dwordx4 v[10:13], v[170:171], off offset:48
	global_load_dwordx4 v[14:17], v[170:171], off offset:32
	global_load_dwordx4 v[30:33], v[170:171], off offset:16
	global_load_dwordx4 v[34:37], v[170:171], off
	v_mov_b32_e32 v122, v112
	v_mov_b32_e32 v123, v4
	v_mov_b32_e32 v4, v113
	global_load_dwordx4 v[70:73], v[170:171], off offset:176
	global_load_dwordx4 v[82:85], v[170:171], off offset:160
	global_load_dwordx4 v[102:105], v[170:171], off offset:144
	global_load_dwordx4 v[110:113], v[170:171], off offset:128
	v_mov_b32_e32 v170, v120
	v_mov_b32_e32 v171, v118
	v_add_f32_e32 v24, v181, v24
	v_pk_mul_f32 v[170:171], v[170:171], v[170:171]
	v_add_f32_e32 v24, v180, v24
	v_add_f32_e32 v24, v171, v24
	v_add_f32_e32 v24, v170, v24
	v_mov_b32_e32 v178, v28
	v_mov_b32_e32 v28, v24
	s_nop 1
	v_permlane32_swap_b32_e32 v24, v28
	v_add_f32_e32 v24, v24, v28
	v_fmamk_f32 v24, v24, 0x3baaaaab, v163
	v_mul_f32_e32 v28, 0x4b800000, v24
	v_cmp_gt_f32_e32 vcc, s69, v24
	s_nop 1
	v_cndmask_b32_e32 v24, v24, v28, vcc
	v_rsq_f32_e32 v170, v24
	v_mov_b32_e32 v24, v29
	v_mov_b32_e32 v29, v22
	v_mov_b32_e32 v28, v26
	v_mul_f32_e32 v22, 0x45800000, v170
	v_cndmask_b32_e32 v22, v170, v22, vcc
	v_mul_f32_e32 v26, 0x3dd53b94, v22
	s_waitcnt vmcnt(22)
	v_mul_f32_e32 v22, v114, v26
	v_mul_f32_e32 v114, v22, v190
	v_mul_f32_e32 v22, v106, v26
	v_mul_f32_e32 v106, v22, v194
	v_mul_f32_e32 v22, v115, v26
	v_mul_f32_e32 v115, v22, v191
	v_mul_f32_e32 v22, v107, v26
	v_mul_f32_e32 v107, v22, v195
	v_mul_f32_e32 v22, v116, v26
	v_mul_f32_e32 v116, v22, v192
	v_mul_f32_e32 v22, v108, v26
	v_mul_f32_e32 v108, v22, v196
	v_mul_f32_e32 v22, v117, v26
	v_mul_f32_e32 v117, v22, v193
	v_mul_f32_e32 v22, v109, v26
	v_mul_f32_e32 v109, v22, v197
	s_waitcnt vmcnt(20)
	v_mul_f32_e32 v22, v98, v26
	v_mul_f32_e32 v170, v22, v198
	v_mul_f32_e32 v22, v94, v26
	v_mul_f32_e32 v94, v22, v202
	v_mul_f32_e32 v22, v99, v26
	v_mul_f32_e32 v171, v22, v199
	v_mul_f32_e32 v22, v95, v26
	v_mul_f32_e32 v95, v22, v203
	v_mul_f32_e32 v22, v100, v26
	v_mul_f32_e32 v172, v22, v200
	v_mul_f32_e32 v22, v96, v26
	v_mul_f32_e32 v96, v22, v204
	v_mul_f32_e32 v22, v101, v26
	v_mul_f32_e32 v173, v22, v201
	v_mul_f32_e32 v22, v97, v26
	v_mul_f32_e32 v97, v22, v205
	s_waitcnt vmcnt(18)
	v_mul_f32_e32 v22, v90, v26
	v_mul_f32_e32 v90, v22, v206
	v_mul_f32_e32 v22, v86, v26
	v_mul_f32_e32 v86, v22, v210
	v_mul_f32_e32 v22, v91, v26
	v_mul_f32_e32 v91, v22, v207
	v_mul_f32_e32 v22, v87, v26
	v_mul_f32_e32 v87, v22, v211
	v_mul_f32_e32 v22, v92, v26
	v_mul_f32_e32 v92, v22, v208
	v_mul_f32_e32 v22, v88, v26
	v_mul_f32_e32 v88, v22, v212
	v_mul_f32_e32 v22, v93, v26
	v_mul_f32_e32 v93, v22, v209
	v_mul_f32_e32 v22, v89, v26
	v_mul_f32_e32 v89, v22, v213
	s_waitcnt vmcnt(16)
	v_mul_f32_e32 v22, v78, v26
	v_mul_f32_e32 v78, v22, v214
	v_mul_f32_e32 v22, v74, v26
	v_mul_f32_e32 v74, v22, v218
	v_mul_f32_e32 v22, v79, v26
	v_mul_f32_e32 v79, v22, v215
	v_mul_f32_e32 v22, v75, v26
	v_mul_f32_e32 v75, v22, v219
	v_mul_f32_e32 v22, v80, v26
	v_mul_f32_e32 v80, v22, v216
	v_mul_f32_e32 v22, v76, v26
	v_mul_f32_e32 v76, v22, v220
	v_mul_f32_e32 v22, v81, v26
	v_mul_f32_e32 v81, v22, v217
	v_mul_f32_e32 v22, v77, v26
	v_mul_f32_e32 v77, v22, v221
	s_waitcnt vmcnt(14)
	v_mul_f32_e32 v22, v66, v26
	v_mul_f32_e32 v66, v22, v222
	v_mul_f32_e32 v22, v26, v62
	v_mul_f32_e32 v62, v22, v226
	v_mul_f32_e32 v22, v67, v26
	v_mul_f32_e32 v67, v22, v223
	v_mul_f32_e32 v22, v26, v63
	v_mul_f32_e32 v63, v22, v227
	v_mul_f32_e32 v22, v68, v26
	v_mul_f32_e32 v68, v22, v224
	v_mul_f32_e32 v22, v26, v64
	v_mul_f32_e32 v64, v22, v228
	v_mul_f32_e32 v22, v69, v26
	v_mul_f32_e32 v69, v22, v225
	v_mul_f32_e32 v22, v26, v65
	v_mul_f32_e32 v65, v22, v229
	s_waitcnt vmcnt(12)
	v_mul_f32_e32 v22, v26, v58
	v_mul_f32_e32 v58, v22, v230
	v_mul_f32_e32 v22, v26, v54
	v_mul_f32_e32 v54, v22, v234
	v_mul_f32_e32 v22, v26, v59
	v_mul_f32_e32 v59, v22, v231
	v_mul_f32_e32 v22, v26, v55
	v_mul_f32_e32 v55, v22, v235
	v_mul_f32_e32 v22, v26, v60
	v_mul_f32_e32 v60, v22, v232
	v_mul_f32_e32 v22, v26, v56
	v_mul_f32_e32 v56, v22, v236
	v_mul_f32_e32 v22, v26, v61
	v_mul_f32_e32 v61, v22, v233
	v_mul_f32_e32 v22, v26, v57
	v_mul_f32_e32 v57, v22, v237
	s_waitcnt vmcnt(10)
	v_mul_f32_e32 v22, v26, v50
	v_mul_f32_e32 v174, v22, v238
	v_mul_f32_e32 v22, v26, v46
	v_mul_f32_e32 v175, v22, v242
	v_mul_f32_e32 v22, v26, v51
	v_mul_f32_e32 v176, v22, v239
	v_mul_f32_e32 v22, v26, v47
	v_mul_f32_e32 v177, v22, v243
	v_mul_f32_e32 v22, v26, v52
	v_mul_f32_e32 v52, v22, v240
	v_mul_f32_e32 v22, v26, v48
	v_mul_f32_e32 v180, v22, v244
	v_mul_f32_e32 v22, v26, v53
	v_mul_f32_e32 v53, v22, v241
	v_mul_f32_e32 v22, v26, v49
	v_mul_f32_e32 v181, v22, v245
	s_waitcnt vmcnt(8)
	v_mul_f32_e32 v22, v26, v42
	v_mul_f32_e32 v182, v22, v246
	v_mul_f32_e32 v22, v26, v38
	v_mul_f32_e32 v183, v22, v250
	v_mul_f32_e32 v22, v26, v43
	v_mul_f32_e32 v190, v22, v247
	v_mul_f32_e32 v22, v26, v39
	v_mul_f32_e32 v191, v22, v251
	v_mul_f32_e32 v22, v26, v44
	v_mul_f32_e32 v192, v22, v248
	v_mul_f32_e32 v22, v26, v40
	v_mul_f32_e32 v193, v22, v252
	v_mul_f32_e32 v22, v26, v45
	v_mul_f32_e32 v194, v22, v249
	v_mul_f32_e32 v22, v26, v41
	v_pk_mul_f32 v[28:29], v[26:27], v[28:29] op_sel_hi:[0,1]
	v_mul_f32_e32 v195, v22, v253
	v_pk_mul_f32 v[28:29], v[28:29], v[186:187]
	v_mov_b32_e32 v22, v27
	v_pk_mul_f32 v[38:39], v[26:27], v[158:159] op_sel_hi:[0,1]
	v_pk_mul_f32 v[22:23], v[26:27], v[22:23] op_sel_hi:[0,1]
	v_pk_mul_f32 v[18:19], v[26:27], v[18:19] op_sel_hi:[0,1]
	v_pk_mul_f32 v[40:41], v[26:27], v[178:179] op_sel_hi:[0,1]
	v_pk_mul_f32 v[42:43], v[26:27], v[150:151] op_sel_hi:[0,1]
	v_pk_mul_f32 v[24:25], v[26:27], v[24:25] op_sel_hi:[0,1]
	v_pk_mul_f32 v[20:21], v[26:27], v[20:21] op_sel_hi:[0,1]
	v_pk_mul_f32 v[44:45], v[26:27], v[140:141] op_sel_hi:[0,1]
	v_pk_mul_f32 v[46:47], v[26:27], v[128:129] op_sel_hi:[0,1]
	v_pk_mul_f32 v[6:7], v[26:27], v[6:7] op_sel_hi:[0,1]
	v_pk_mul_f32 v[2:3], v[26:27], v[2:3] op_sel_hi:[0,1]
	v_pk_mul_f32 v[48:49], v[26:27], v[134:135] op_sel_hi:[0,1]
	v_pk_mul_f32 v[50:51], v[26:27], v[122:123] op_sel_hi:[0,1]
	v_pk_mul_f32 v[8:9], v[26:27], v[8:9] op_sel_hi:[0,1]
	v_pk_mul_f32 v[4:5], v[26:27], v[4:5] op_sel_hi:[0,1]
	s_waitcnt vmcnt(4)
	v_pk_mul_f32 v[26:27], v[28:29], v[34:35] op_sel:[1,0] op_sel_hi:[0,1]
	v_pk_mul_f32 v[22:23], v[22:23], v[188:189]
	v_pk_mul_f32 v[48:49], v[48:49], v[130:131]
	v_sub_f32_e32 v130, v26, v27
	v_pk_mul_f32 v[26:27], v[28:29], v[34:35]
	v_pk_mul_f32 v[40:41], v[40:41], v[156:157]
	v_add_f32_e32 v28, v27, v26
	v_pk_mul_f32 v[26:27], v[22:23], v[36:37] op_sel:[1,0] op_sel_hi:[0,1]
	v_pk_mul_f32 v[22:23], v[22:23], v[36:37]
	v_sub_f32_e32 v26, v26, v27
	v_add_f32_e32 v27, v23, v22
	v_pk_mul_f32 v[22:23], v[40:41], v[30:31] op_sel:[1,0] op_sel_hi:[0,1]
	v_pk_mul_f32 v[24:25], v[24:25], v[184:185]
	v_sub_f32_e32 v29, v22, v23
	v_pk_mul_f32 v[22:23], v[40:41], v[30:31]
	v_pk_mul_f32 v[38:39], v[38:39], v[152:153]
	v_add_f32_e32 v30, v23, v22
	v_pk_mul_f32 v[22:23], v[24:25], v[32:33] op_sel:[1,0] op_sel_hi:[0,1]
	v_sub_f32_e32 v31, v22, v23
	v_pk_mul_f32 v[22:23], v[24:25], v[32:33]
	v_pk_mul_f32 v[18:19], v[18:19], v[154:155]
	v_add_f32_e32 v24, v23, v22
	v_pk_mul_f32 v[22:23], v[38:39], v[14:15] op_sel:[1,0] op_sel_hi:[0,1]
	v_pk_mul_f32 v[14:15], v[38:39], v[14:15]
	v_sub_f32_e32 v22, v22, v23
	v_add_f32_e32 v23, v15, v14
	v_pk_mul_f32 v[14:15], v[18:19], v[16:17] op_sel:[1,0] op_sel_hi:[0,1]
	v_pk_mul_f32 v[42:43], v[42:43], v[142:143]
	v_sub_f32_e32 v25, v14, v15
	v_pk_mul_f32 v[14:15], v[18:19], v[16:17]
	v_pk_mul_f32 v[20:21], v[20:21], v[144:145]
	v_add_f32_e32 v16, v15, v14
	v_pk_mul_f32 v[14:15], v[42:43], v[10:11] op_sel:[1,0] op_sel_hi:[0,1]
	v_pk_mul_f32 v[10:11], v[42:43], v[10:11]
	v_sub_f32_e32 v14, v14, v15
	v_add_f32_e32 v15, v11, v10
	v_pk_mul_f32 v[10:11], v[20:21], v[12:13] op_sel:[1,0] op_sel_hi:[0,1]
	v_pk_mul_f32 v[44:45], v[44:45], v[136:137]
	v_sub_f32_e32 v17, v10, v11
	v_pk_mul_f32 v[10:11], v[20:21], v[12:13]
	v_pk_mul_f32 v[6:7], v[6:7], v[138:139]
	v_add_f32_e32 v12, v11, v10
	s_waitcnt vmcnt(0)
	v_pk_mul_f32 v[10:11], v[44:45], v[110:111] op_sel:[1,0] op_sel_hi:[0,1]
	v_sub_f32_e32 v13, v10, v11
	v_pk_mul_f32 v[10:11], v[44:45], v[110:111]
	v_pk_mul_f32 v[8:9], v[8:9], v[132:133]
	v_add_f32_e32 v18, v11, v10
	v_pk_mul_f32 v[10:11], v[6:7], v[112:113] op_sel:[1,0] op_sel_hi:[0,1]
	v_pk_mul_f32 v[6:7], v[6:7], v[112:113]
	v_sub_f32_e32 v10, v10, v11
	v_add_f32_e32 v11, v7, v6
	v_pk_mul_f32 v[6:7], v[48:49], v[102:103] op_sel:[1,0] op_sel_hi:[0,1]
	v_sub_f32_e32 v19, v6, v7
	v_pk_mul_f32 v[6:7], v[48:49], v[102:103]
	v_pk_mul_f32 v[46:47], v[46:47], v[124:125]
	v_add_f32_e32 v20, v7, v6
	v_pk_mul_f32 v[6:7], v[8:9], v[104:105] op_sel:[1,0] op_sel_hi:[0,1]
	v_sub_f32_e32 v21, v6, v7
	v_pk_mul_f32 v[6:7], v[8:9], v[104:105]
	v_pk_mul_f32 v[2:3], v[2:3], v[126:127]
	v_add_f32_e32 v8, v7, v6
	v_pk_mul_f32 v[6:7], v[46:47], v[82:83] op_sel:[1,0] op_sel_hi:[0,1]
	v_sub_f32_e32 v9, v6, v7
	v_pk_mul_f32 v[6:7], v[46:47], v[82:83]
	v_pk_mul_f32 v[50:51], v[50:51], v[118:119]
	v_add_f32_e32 v32, v7, v6
	v_pk_mul_f32 v[6:7], v[2:3], v[84:85] op_sel:[1,0] op_sel_hi:[0,1]
	v_pk_mul_f32 v[2:3], v[2:3], v[84:85]
	v_sub_f32_e32 v6, v6, v7
	v_add_f32_e32 v7, v3, v2
	v_pk_mul_f32 v[2:3], v[50:51], v[70:71] op_sel:[1,0] op_sel_hi:[0,1]
	v_pk_mul_f32 v[4:5], v[4:5], v[120:121]
	v_sub_f32_e32 v33, v2, v3
	v_pk_mul_f32 v[2:3], v[50:51], v[70:71]
	v_cvt_pk_bf16_f32 v98, v114, v115
	v_cvt_pk_bf16_f32 v99, v116, v117
	v_cvt_pk_bf16_f32 v100, v106, v107
	v_cvt_pk_bf16_f32 v101, v108, v109
	v_cvt_pk_bf16_f32 v102, v170, v171
	s_nop 0
	v_add_f32_e32 v34, v3, v2
	v_pk_mul_f32 v[2:3], v[4:5], v[72:73] op_sel:[1,0] op_sel_hi:[0,1]
	v_sub_f32_e32 v35, v2, v3
	v_pk_mul_f32 v[2:3], v[4:5], v[72:73]
	v_cvt_pk_bf16_f32 v103, v172, v173
	v_cvt_pk_bf16_f32 v104, v94, v95
	v_cvt_pk_bf16_f32 v105, v96, v97
	v_cvt_pk_bf16_f32 v106, v90, v91
	v_cvt_pk_bf16_f32 v107, v92, v93
	s_nop 0
	v_add_f32_e32 v2, v3, v2
	v_cvt_pk_bf16_f32 v108, v86, v87
	v_cvt_pk_bf16_f32 v109, v88, v89
	v_cvt_pk_bf16_f32 v110, v78, v79
	v_cvt_pk_bf16_f32 v111, v80, v81
	v_cvt_pk_bf16_f32 v112, v74, v75
	v_cvt_pk_bf16_f32 v113, v76, v77
	v_cvt_pk_bf16_f32 v114, v66, v67
	v_cvt_pk_bf16_f32 v115, v68, v69
	v_cvt_pk_bf16_f32 v116, v62, v63
	v_cvt_pk_bf16_f32 v117, v64, v65
	v_cvt_pk_bf16_f32 v118, v58, v59
	v_cvt_pk_bf16_f32 v119, v60, v61
	v_cvt_pk_bf16_f32 v120, v54, v55
	v_cvt_pk_bf16_f32 v121, v56, v57
	v_cvt_pk_bf16_f32 v122, v174, v176
	v_cvt_pk_bf16_f32 v123, v52, v53
	v_cvt_pk_bf16_f32 v124, v175, v177
	v_cvt_pk_bf16_f32 v125, v180, v181
	v_cvt_pk_bf16_f32 v126, v182, v190
	v_cvt_pk_bf16_f32 v127, v192, v194
	v_cvt_pk_bf16_f32 v128, v183, v191
	v_cvt_pk_bf16_f32 v129, v193, v195
	v_cvt_pk_bf16_f32 v130, v130, v26
	v_cvt_pk_bf16_f32 v131, v29, v31
	v_cvt_pk_bf16_f32 v132, v22, v25
	v_cvt_pk_bf16_f32 v133, v14, v17
	v_cvt_pk_bf16_f32 v134, v13, v10
	v_cvt_pk_bf16_f32 v135, v19, v21
	v_cvt_pk_bf16_f32 v136, v9, v6
	v_cvt_pk_bf16_f32 v137, v33, v35
	v_cvt_pk_bf16_f32 v138, v28, v27
	v_cvt_pk_bf16_f32 v139, v30, v24
	v_cvt_pk_bf16_f32 v140, v23, v16
	v_cvt_pk_bf16_f32 v141, v15, v12
	v_cvt_pk_bf16_f32 v142, v18, v11
	v_cvt_pk_bf16_f32 v143, v20, v8
	v_cvt_pk_bf16_f32 v144, v32, v7
	v_cvt_pk_bf16_f32 v145, v34, v2
	v_mul_hi_i32 v2, v168, s70
	v_lshrrev_b32_e32 v3, 31, v2
	v_ashrrev_i32_e32 v2, 2, v2
	v_add_u32_e32 v2, v2, v3
	v_mul_lo_u32 v3, v2, 24
	v_sub_u32_e32 v3, v168, v3
	v_lshrrev_b32_e32 v16, 1, v2
	v_bitop3_b32 v3, v16, v3, 7 bitop3:0x6c
	v_mul_lo_u32 v2, v2, s68
	v_lshl_add_u32 v2, v3, 4, v2
	v_add_u32_e32 v3, 0x200, v168
	v_mul_hi_i32 v4, v3, s70
	v_lshrrev_b32_e32 v5, 31, v4
	v_ashrrev_i32_e32 v4, 2, v4
	v_add_u32_e32 v4, v4, v5
	v_mul_lo_u32 v5, v4, 24
	v_sub_u32_e32 v5, v3, v5
	v_lshrrev_b32_e32 v16, 1, v4
	v_bitop3_b32 v5, v16, v5, 7 bitop3:0x6c
	v_mul_lo_u32 v4, v4, s68
	v_lshl_add_u32 v4, v5, 4, v4
	v_add_u32_e32 v5, 0x400, v168
	v_mul_hi_i32 v6, v5, s70
	v_lshrrev_b32_e32 v7, 31, v6
	v_ashrrev_i32_e32 v6, 2, v6
	v_add_u32_e32 v6, v6, v7
	v_mul_lo_u32 v7, v6, 24
	v_sub_u32_e32 v5, v5, v7
	v_lshrrev_b32_e32 v16, 1, v6
	v_bitop3_b32 v5, v16, v5, 7 bitop3:0x6c
	v_mul_lo_u32 v6, v6, s68
	v_ashrrev_i32_e32 v9, 4, v168
	v_lshl_add_u32 v6, v5, 4, v6
	v_bfe_u32 v5, v168, 2, 2
	v_lshrrev_b32_e32 v7, 1, v168
	v_and_b32_e32 v10, 0x1ffff0, v9
	v_lshrrev_b32_e32 v9, 1, v9
	v_ashrrev_i32_e32 v3, 4, v3
	v_and_or_b32 v5, v7, 8, v5
	v_and_b32_e32 v7, 0x60, v168
	v_lshlrev_b32_e32 v8, 3, v168
	v_and_b32_e32 v9, 4, v9
	v_and_b32_e32 v11, 0x1ffff0, v3
	v_lshrrev_b32_e32 v3, 1, v3
	v_and_or_b32 v7, v8, 24, v7
	v_or3_b32 v9, v10, v9, v5
	v_and_b32_e32 v3, 4, v3
	s_barrier
	global_load_lds_dwordx4 v2, s[44:45]
	s_mov_b32 m0, s72
	v_lshlrev_b32_e32 v7, 1, v7
	v_lshlrev_b32_e32 v10, 11, v9
	v_or3_b32 v3, v11, v3, v5
	global_load_lds_dwordx4 v4, s[44:45]
	s_mov_b32 m0, s73
	v_or_b32_e32 v9, v10, v7
	v_lshlrev_b32_e32 v11, 11, v3
	global_load_lds_dwordx4 v6, s[44:45]
	s_mov_b32 m0, s64
	v_or_b32_e32 v3, v11, v7
	global_load_lds_dwordx4 v9, s[46:47]
	s_mov_b32 m0, s74
	v_lshlrev_b32_e32 v13, 1, v168
	global_load_lds_dwordx4 v3, s[46:47]
	v_lshlrev_b32_e32 v9, 4, v168
	v_and_b32_e32 v14, 32, v13
	v_or_b32_e32 v3, 32, v148
	v_mul_u32_u24_e32 v5, 0x180, v167
	v_and_b32_e32 v7, 0x70, v8
	v_and_b32_e32 v12, 0xc0, v9
	v_and_or_b32 v8, v8, s75, v14
	v_bitop3_b32 v172, v3, v5, v7 bitop3:0xde
	v_or_b32_e32 v3, 64, v148
	v_mul_i32_i24_e32 v15, -4, v169
	v_add3_u32 v169, v12, 0, v8
	v_and_b32_e32 v12, 0xc0, v13
	v_and_b32_e32 v13, 48, v9
	v_bitop3_b32 v173, v3, v5, v7 bitop3:0xde
	v_or_b32_e32 v3, 0x60, v148
	v_or3_b32 v8, v11, v12, v13
	v_mov_b32_e32 v9, v149
	v_bitop3_b32 v171, v148, v5, v7 bitop3:0xde
	v_bitop3_b32 v174, v3, v5, v7 bitop3:0xde
	v_mov_b32_e32 v3, v149
	v_mov_b32_e32 v5, v149
	v_mov_b32_e32 v7, v149
	v_lshl_add_u64 v[150:151], s[48:49], 0, v[8:9]
	v_or3_b32 v8, v10, v12, v13
	v_mov_b32_e32 v16, v149
	v_mov_b32_e32 v17, v149
	v_and_b32_e32 v170, 63, v168
	s_lshl_b32 s46, s80, 2
	v_lshl_add_u32 v168, v167, 2, s65
	v_lshl_add_u64 v[152:153], s[48:49], 0, v[8:9]
	v_lshl_add_u64 v[154:155], s[50:51], 0, v[6:7]
	v_lshl_add_u64 v[156:157], s[50:51], 0, v[4:5]
	v_lshl_add_u64 v[158:159], s[50:51], 0, v[2:3]
	v_add3_u32 v167, s63, v15, v167
	v_mov_b32_e32 v2, v149
	v_mov_b32_e32 v4, v149
	v_mov_b32_e32 v6, v149
	v_mov_b32_e32 v8, v149
	v_mov_b32_e32 v10, v149
	v_mov_b32_e32 v11, v149
	v_mov_b32_e32 v12, v149
	v_mov_b32_e32 v13, v149
	v_mov_b32_e32 v14, v149
	v_mov_b32_e32 v15, v149
	v_mov_b64_e32 v[32:33], v[16:17]
	v_mov_b64_e32 v[48:49], v[16:17]
	v_mov_b64_e32 v[64:65], v[16:17]
	s_add_i32 s46, s46, 4
	v_cmp_gt_u32_e64 s[0:1], 32, v170
	v_mov_b32_e32 v176, 0
	v_mov_b32_e32 v175, 0
	v_mov_b32_e32 v210, 0
	v_mov_b32_e32 v211, 0
	v_mov_b32_e32 v212, 0
	v_mov_b32_e32 v213, 0
	v_mov_b32_e32 v214, 0
	v_mov_b32_e32 v215, 0
	v_mov_b32_e32 v216, 0
	v_mov_b32_e32 v217, 0
	v_mov_b32_e32 v218, 0
	v_mov_b32_e32 v219, 0
	v_mov_b32_e32 v220, 0
	v_mov_b32_e32 v221, 0
	v_mov_b32_e32 v222, 0
	v_mov_b32_e32 v223, 0
	v_mov_b32_e32 v224, 0
	v_mov_b32_e32 v225, 0
	s_movk_i32 s47, 0xff00
	v_mov_b64_e32 v[30:31], v[14:15]
	v_mov_b64_e32 v[28:29], v[12:13]
	v_mov_b64_e32 v[26:27], v[10:11]
	v_mov_b64_e32 v[24:25], v[8:9]
	v_mov_b64_e32 v[22:23], v[6:7]
	v_mov_b64_e32 v[20:21], v[4:5]
	v_mov_b64_e32 v[18:19], v[2:3]
	v_mov_b64_e32 v[46:47], v[14:15]
	v_mov_b64_e32 v[44:45], v[12:13]
	v_mov_b64_e32 v[42:43], v[10:11]
	v_mov_b64_e32 v[40:41], v[8:9]
	v_mov_b64_e32 v[38:39], v[6:7]
	v_mov_b64_e32 v[36:37], v[4:5]
	v_mov_b64_e32 v[34:35], v[2:3]
	v_mov_b64_e32 v[62:63], v[14:15]
	v_mov_b64_e32 v[60:61], v[12:13]
	v_mov_b64_e32 v[58:59], v[10:11]
	v_mov_b64_e32 v[56:57], v[8:9]
	v_mov_b64_e32 v[54:55], v[6:7]
	v_mov_b64_e32 v[52:53], v[4:5]
	v_mov_b64_e32 v[50:51], v[2:3]

.LBB0_948:
	s_mul_i32 s44, s48, 0x6000
	s_add_i32 s44, s44, 0
	s_add_i32 s44, s44, 0x8000
	v_add_u32_e32 v177, s44, v171
	ds_read_b128 v[66:69], v177 offset:0
	ds_read_b128 v[82:85], v177 offset:0x3000
	v_add_u32_e32 v206, s44, v172
	ds_read_b128 v[178:181], v206 offset:0
	ds_read_b128 v[182:185], v206 offset:0x3000
	v_add_u32_e32 v207, s44, v173
	ds_read_b128 v[186:189], v207 offset:0
	ds_read_b128 v[190:193], v207 offset:0x3000
	s_waitcnt lgkmcnt(4)
	v_add_u32_e32 v208, s44, v174
	v_mfma_f32_32x32x16_bf16 v[66:81], v[66:69], v[98:101], v[210:225]
	ds_read_b128 v[194:197], v208 offset:0
	ds_read_b128 v[198:201], v208 offset:0x3000
	s_waitcnt lgkmcnt(4)
	v_mfma_f32_32x32x16_bf16 v[82:97], v[82:85], v[98:101], v[210:225]
	v_mfma_f32_32x32x16_bf16 v[66:81], v[178:181], v[102:105], v[66:81]
	ds_read_b128 v[178:181], v177 offset:0x80
	ds_read_b128 v[202:205], v177 offset:0x3080
	s_waitcnt lgkmcnt(4)
	v_mfma_f32_32x32x16_bf16 v[82:97], v[182:185], v[102:105], v[82:97]
	v_mfma_f32_32x32x16_bf16 v[66:81], v[186:189], v[106:109], v[66:81]
	ds_read_b128 v[182:185], v206 offset:0x80
	ds_read_b128 v[186:189], v206 offset:0x3080
	s_waitcnt lgkmcnt(4)
	v_mfma_f32_32x32x16_bf16 v[82:97], v[190:193], v[106:109], v[82:97]
	v_mfma_f32_32x32x16_bf16 v[66:81], v[194:197], v[110:113], v[66:81]
	ds_read_b128 v[190:193], v207 offset:0x80
	ds_read_b128 v[194:197], v207 offset:0x3080
	s_waitcnt lgkmcnt(4)
	v_mfma_f32_32x32x16_bf16 v[82:97], v[198:201], v[110:113], v[82:97]
	v_mfma_f32_32x32x16_bf16 v[66:81], v[178:181], v[114:117], v[66:81]
	ds_read_b128 v[178:181], v208 offset:0x80
	ds_read_b128 v[198:201], v208 offset:0x3080
	s_waitcnt lgkmcnt(4)
	v_mfma_f32_32x32x16_bf16 v[82:97], v[202:205], v[114:117], v[82:97]
	v_mfma_f32_32x32x16_bf16 v[66:81], v[182:185], v[118:121], v[66:81]
	ds_read_b128 v[182:185], v177 offset:0x100
	ds_read_b128 v[202:205], v177 offset:0x3100
	s_waitcnt lgkmcnt(4)
	v_mfma_f32_32x32x16_bf16 v[82:97], v[186:189], v[118:121], v[82:97]
	v_mfma_f32_32x32x16_bf16 v[66:81], v[190:193], v[122:125], v[66:81]
	ds_read_b128 v[186:189], v206 offset:0x100
	ds_read_b128 v[190:193], v206 offset:0x3100
	s_waitcnt lgkmcnt(4)
	v_mfma_f32_32x32x16_bf16 v[82:97], v[194:197], v[122:125], v[82:97]
	v_mfma_f32_32x32x16_bf16 v[66:81], v[178:181], v[126:129], v[66:81]
	ds_read_b128 v[178:181], v207 offset:0x100
	ds_read_b128 v[194:197], v207 offset:0x3100
	s_waitcnt lgkmcnt(4)
	v_mfma_f32_32x32x16_bf16 v[82:97], v[198:201], v[126:129], v[82:97]
	v_mfma_f32_32x32x16_bf16 v[66:81], v[182:185], v[130:133], v[66:81]
	ds_read_b128 v[182:185], v208 offset:0x100
	ds_read_b128 v[198:201], v208 offset:0x3100
	s_waitcnt lgkmcnt(4)
	v_mfma_f32_32x32x16_bf16 v[82:97], v[202:205], v[130:133], v[82:97]
	v_mfma_f32_32x32x16_bf16 v[66:81], v[186:189], v[134:137], v[66:81]
	s_waitcnt lgkmcnt(2)
	v_mfma_f32_32x32x16_bf16 v[82:97], v[190:193], v[134:137], v[82:97]
	v_mfma_f32_32x32x16_bf16 v[66:81], v[178:181], v[138:141], v[66:81]
	s_waitcnt lgkmcnt(0)
	v_mfma_f32_32x32x16_bf16 v[82:97], v[194:197], v[138:141], v[82:97]
	v_mfma_f32_32x32x16_bf16 v[66:81], v[182:185], v[142:145], v[66:81]
	s_add_i32 s44, s47, 0x13f
	s_cmp_le_i32 s44, s55
	v_mfma_f32_32x32x16_bf16 v[82:97], v[198:201], v[142:145], v[82:97]
	s_cbranch_scc1 .LBB0_950
	v_add_u32_e32 v177, s54, v167
	v_cmp_lt_i32_e32 vcc, -1, v177
	v_add_u32_e32 v178, -1, v177
	s_nop 4
	v_cndmask_b32_e32 v66, v165, v66, vcc
	v_cmp_lt_i32_e32 vcc, 31, v177
	s_nop 1
	v_cndmask_b32_e32 v82, v165, v82, vcc
	v_cmp_lt_i32_e32 vcc, -1, v178
	s_nop 1
	v_cndmask_b32_e32 v67, v165, v67, vcc
	v_cmp_lt_i32_e32 vcc, 31, v178
	v_add_u32_e32 v178, -2, v177
	s_nop 0
	v_cndmask_b32_e32 v83, v165, v83, vcc
	v_cmp_lt_i32_e32 vcc, -1, v178
	s_nop 1
	v_cndmask_b32_e32 v68, v165, v68, vcc
	v_cmp_lt_i32_e32 vcc, 31, v178
	v_add_u32_e32 v178, -3, v177
	s_nop 0
	v_cndmask_b32_e32 v84, v165, v84, vcc
	v_cmp_lt_i32_e32 vcc, -1, v178
	s_nop 1
	v_cndmask_b32_e32 v69, v165, v69, vcc
	v_cmp_lt_i32_e32 vcc, 31, v178
	v_add_u32_e32 v178, -8, v177
	s_nop 0
	v_cndmask_b32_e32 v85, v165, v85, vcc
	v_cmp_lt_i32_e32 vcc, -1, v178
	s_nop 1
	v_cndmask_b32_e32 v70, v165, v70, vcc
	v_cmp_lt_i32_e32 vcc, 31, v178
	v_add_u32_e32 v178, -9, v177
	s_nop 0
	v_cndmask_b32_e32 v86, v165, v86, vcc
	v_cmp_lt_i32_e32 vcc, -1, v178
	s_nop 1
	v_cndmask_b32_e32 v71, v165, v71, vcc
	v_cmp_lt_i32_e32 vcc, 31, v178
	v_add_u32_e32 v178, -10, v177
	s_nop 0
	v_cndmask_b32_e32 v87, v165, v87, vcc
	v_cmp_lt_i32_e32 vcc, -1, v178
	s_nop 1
	v_cndmask_b32_e32 v72, v165, v72, vcc
	v_cmp_lt_i32_e32 vcc, 31, v178
	v_add_u32_e32 v178, -11, v177
	s_nop 0
	v_cndmask_b32_e32 v88, v165, v88, vcc
	v_cmp_lt_i32_e32 vcc, -1, v178
	s_nop 1
	v_cndmask_b32_e32 v73, v165, v73, vcc
	v_cmp_lt_i32_e32 vcc, 31, v178
	v_add_u32_e32 v178, -16, v177
	s_nop 0
	v_cndmask_b32_e32 v89, v165, v89, vcc
	v_cmp_lt_i32_e32 vcc, -1, v178
	s_nop 1
	v_cndmask_b32_e32 v74, v165, v74, vcc
	v_cmp_lt_i32_e32 vcc, 31, v178
	v_subrev_u32_e32 v178, 17, v177
	s_nop 0
	v_cndmask_b32_e32 v90, v165, v90, vcc
	v_cmp_lt_i32_e32 vcc, -1, v178
	s_nop 1
	v_cndmask_b32_e32 v75, v165, v75, vcc
	v_cmp_lt_i32_e32 vcc, 31, v178
	v_subrev_u32_e32 v178, 18, v177
	s_nop 0
	v_cndmask_b32_e32 v91, v165, v91, vcc
	v_cmp_lt_i32_e32 vcc, -1, v178
	s_nop 1
	v_cndmask_b32_e32 v76, v165, v76, vcc
	v_cmp_lt_i32_e32 vcc, 31, v178
	v_subrev_u32_e32 v178, 19, v177
	s_nop 0
	v_cndmask_b32_e32 v92, v165, v92, vcc
	v_cmp_lt_i32_e32 vcc, -1, v178
	s_nop 1
	v_cndmask_b32_e32 v77, v165, v77, vcc
	v_cmp_lt_i32_e32 vcc, 31, v178
	v_subrev_u32_e32 v178, 24, v177
	s_nop 0
	v_cndmask_b32_e32 v93, v165, v93, vcc
	v_cmp_lt_i32_e32 vcc, -1, v178
	s_nop 1
	v_cndmask_b32_e32 v78, v165, v78, vcc
	v_cmp_lt_i32_e32 vcc, 31, v178
	v_subrev_u32_e32 v178, 25, v177
	s_nop 0
	v_cndmask_b32_e32 v94, v165, v94, vcc
	v_cmp_lt_i32_e32 vcc, -1, v178
	s_nop 1
	v_cndmask_b32_e32 v79, v165, v79, vcc
	v_cmp_lt_i32_e32 vcc, 31, v178
	v_subrev_u32_e32 v178, 26, v177
	v_subrev_u32_e32 v177, 27, v177
	v_cndmask_b32_e32 v95, v165, v95, vcc
	v_cmp_lt_i32_e32 vcc, -1, v178
	s_nop 1
	v_cndmask_b32_e32 v80, v165, v80, vcc
	v_cmp_lt_i32_e32 vcc, 31, v178
	s_nop 1
	v_cndmask_b32_e32 v96, v165, v96, vcc
	v_cmp_lt_i32_e32 vcc, -1, v177
	s_nop 1
	v_cndmask_b32_e32 v81, v165, v81, vcc
	v_cmp_lt_i32_e32 vcc, 31, v177
	s_nop 1
	v_cndmask_b32_e32 v97, v165, v97, vcc
.LBB0_950:
	s_nop 7
	v_max_f32_e32 v177, v67, v67
	v_max_f32_e32 v178, v66, v66
	v_max_f32_e32 v177, v178, v177
	v_max3_f32 v177, v177, v68, v69
	v_max3_f32 v177, v177, v70, v71
	v_max3_f32 v177, v177, v72, v73
	v_max3_f32 v177, v177, v74, v75
	v_max3_f32 v177, v177, v76, v77
	v_max3_f32 v177, v177, v78, v79
	v_max3_f32 v177, v177, v80, v81
	v_max3_f32 v177, v177, v82, v83
	v_max3_f32 v177, v177, v84, v85
	v_max3_f32 v177, v177, v86, v87
	v_max3_f32 v177, v177, v88, v89
	v_max3_f32 v177, v177, v90, v91
	v_max3_f32 v177, v177, v92, v93
	v_max3_f32 v177, v177, v94, v95
	v_max3_f32 v177, v177, v96, v97
	v_mov_b32_e32 v178, v177
	s_nop 1
	v_permlane32_swap_b32_e32 v177, v178
	v_max_f32_e32 v178, v178, v178
	v_max_f32_e32 v177, v177, v177
	v_max_f32_e32 v177, v177, v178
	v_cmp_ge_f32_e32 vcc, s76, v177
	s_cmp_eq_u64 vcc, exec
	s_cbranch_scc0 .Lsm2_slow
	v_mov_b32_e32 v226, 1.0
.Lsm2_join:
	v_exp_f32_e32 v177, v66
	v_exp_f32_e32 v66, v82
	v_exp_f32_e32 v178, v67
	v_exp_f32_e32 v67, v83
	v_exp_f32_e32 v83, v68
	v_exp_f32_e32 v68, v84
	v_add_f32_e32 v82, v66, v177
	v_add_f32_e32 v82, 0, v82
	v_add_f32_e32 v179, v67, v178
	v_exp_f32_e32 v84, v69
	v_add_f32_e32 v82, v179, v82
	v_mov_b32_e32 v69, v85
	v_add_f32_e32 v85, v68, v83
	v_exp_f32_e32 v69, v69
	v_add_f32_e32 v82, v85, v82
	v_exp_f32_e32 v85, v70
	v_exp_f32_e32 v70, v86
	v_add_f32_e32 v179, v69, v84
	v_exp_f32_e32 v86, v71
	v_add_f32_e32 v82, v179, v82
	v_mov_b32_e32 v71, v87
	v_add_f32_e32 v87, v70, v85
	v_exp_f32_e32 v71, v71
	v_add_f32_e32 v181, v87, v82
	v_exp_f32_e32 v87, v72
	v_exp_f32_e32 v72, v88
	v_add_f32_e32 v182, v71, v86
	v_exp_f32_e32 v179, v73
	v_exp_f32_e32 v82, v89
	v_add_f32_e32 v73, v182, v181
	v_add_f32_e32 v88, v72, v87
	v_add_f32_e32 v181, v88, v73
	v_exp_f32_e32 v88, v74
	v_exp_f32_e32 v73, v90
	v_add_f32_e32 v182, v82, v179
	v_mov_b32_e32 v74, v75
	v_add_f32_e32 v75, v182, v181
	v_add_f32_e32 v90, v73, v88
	v_exp_f32_e32 v89, v74
	v_add_f32_e32 v181, v90, v75
	v_exp_f32_e32 v74, v91
	v_exp_f32_e32 v90, v76
	v_exp_f32_e32 v75, v92
	v_add_f32_e32 v182, v74, v89
	v_mov_b32_e32 v76, v77
	v_add_f32_e32 v77, v182, v181
	v_add_f32_e32 v92, v75, v90
	v_exp_f32_e32 v91, v76
	v_add_f32_e32 v181, v92, v77
	v_exp_f32_e32 v76, v93
	v_exp_f32_e32 v92, v78
	v_exp_f32_e32 v77, v94
	v_add_f32_e32 v182, v76, v91
	v_mov_b32_e32 v78, v79
	v_add_f32_e32 v79, v182, v181
	v_add_f32_e32 v94, v77, v92
	v_exp_f32_e32 v93, v78
	v_add_f32_e32 v181, v94, v79
	v_exp_f32_e32 v78, v95
	v_exp_f32_e32 v94, v80
	v_exp_f32_e32 v79, v96
	v_exp_f32_e32 v95, v81
	v_exp_f32_e32 v80, v97
	v_add_f32_e32 v182, v78, v93
	v_add_f32_e32 v81, v182, v181
	v_add_f32_e32 v96, v79, v94
	v_add_f32_e32 v81, v96, v81
	v_add_f32_e32 v96, v80, v95
	v_add_f32_e32 v81, v96, v81
	v_mov_b32_e32 v96, v226
	v_mov_b32_e32 v97, v81
	s_nop 1
	v_permlane32_swap_b32_e32 v81, v97
	v_cmp_gt_f32_e32 vcc, 1.0, v96


	s_cbranch_vccz .LBB0_954
	s_and_saveexec_b64 s[44:45], s[0:1]
	ds_write_b32 v168, v96
	s_or_b64 exec, exec, s[44:45]
	s_waitcnt lgkmcnt(0)
	v_add_u32_e32 v192, s65, v148
	ds_read_b128 v[180:183], v192 offset:96
	ds_read_b128 v[184:187], v192 offset:64
	ds_read_b128 v[188:191], v192 offset:32
	ds_read_b128 v[192:195], v192
	s_waitcnt lgkmcnt(0)
	v_pk_mul_f32 v[62:63], v[62:63], v[180:181]
	v_pk_mul_f32 v[58:59], v[58:59], v[184:185]
	v_pk_mul_f32 v[54:55], v[54:55], v[188:189]
	v_pk_mul_f32 v[64:65], v[64:65], v[182:183]
	v_pk_mul_f32 v[60:61], v[60:61], v[186:187]
	v_pk_mul_f32 v[56:57], v[56:57], v[190:191]
	v_pk_mul_f32 v[52:53], v[52:53], v[194:195]
	v_pk_mul_f32 v[50:51], v[50:51], v[192:193]
	v_pk_mul_f32 v[46:47], v[46:47], v[180:181]
	v_pk_mul_f32 v[42:43], v[42:43], v[184:185]
	v_pk_mul_f32 v[38:39], v[38:39], v[188:189]
	v_pk_mul_f32 v[48:49], v[48:49], v[182:183]
	v_pk_mul_f32 v[44:45], v[44:45], v[186:187]
	v_pk_mul_f32 v[40:41], v[40:41], v[190:191]
	v_pk_mul_f32 v[36:37], v[36:37], v[194:195]
	v_pk_mul_f32 v[34:35], v[34:35], v[192:193]
	v_pk_mul_f32 v[30:31], v[30:31], v[180:181]
	v_pk_mul_f32 v[26:27], v[26:27], v[184:185]
	v_pk_mul_f32 v[22:23], v[22:23], v[188:189]
	v_pk_mul_f32 v[32:33], v[32:33], v[182:183]
	v_pk_mul_f32 v[28:29], v[28:29], v[186:187]
	v_pk_mul_f32 v[24:25], v[24:25], v[190:191]
	v_pk_mul_f32 v[20:21], v[20:21], v[194:195]
	v_pk_mul_f32 v[18:19], v[18:19], v[192:193]
	v_pk_mul_f32 v[14:15], v[14:15], v[180:181]
	v_pk_mul_f32 v[10:11], v[10:11], v[184:185]
	v_pk_mul_f32 v[6:7], v[6:7], v[188:189]
	v_pk_mul_f32 v[16:17], v[16:17], v[182:183]
	v_pk_mul_f32 v[12:13], v[12:13], v[186:187]
	v_pk_mul_f32 v[8:9], v[8:9], v[190:191]
	v_pk_mul_f32 v[4:5], v[4:5], v[194:195]
	v_pk_mul_f32 v[2:3], v[2:3], v[192:193]

.Lsm2_slow:
	v_max_f32_e32 v177, 0, v177
	v_sub_f32_e32 v66, v66, v177
	v_sub_f32_e32 v67, v67, v177
	v_sub_f32_e32 v68, v68, v177
	v_sub_f32_e32 v69, v69, v177
	v_sub_f32_e32 v70, v70, v177
	v_sub_f32_e32 v71, v71, v177
	v_sub_f32_e32 v72, v72, v177
	v_sub_f32_e32 v73, v73, v177
	v_sub_f32_e32 v74, v74, v177
	v_sub_f32_e32 v75, v75, v177
	v_sub_f32_e32 v76, v76, v177
	v_sub_f32_e32 v77, v77, v177
	v_sub_f32_e32 v78, v78, v177
	v_sub_f32_e32 v79, v79, v177
	v_sub_f32_e32 v80, v80, v177
	v_sub_f32_e32 v81, v81, v177
	v_sub_f32_e32 v82, v82, v177
	v_sub_f32_e32 v83, v83, v177
	v_sub_f32_e32 v84, v84, v177
	v_sub_f32_e32 v85, v85, v177
	v_sub_f32_e32 v86, v86, v177
	v_sub_f32_e32 v87, v87, v177
	v_sub_f32_e32 v88, v88, v177
	v_sub_f32_e32 v89, v89, v177
	v_sub_f32_e32 v90, v90, v177
	v_sub_f32_e32 v91, v91, v177
	v_sub_f32_e32 v92, v92, v177
	v_sub_f32_e32 v93, v93, v177
	v_sub_f32_e32 v94, v94, v177
	v_sub_f32_e32 v95, v95, v177
	v_sub_f32_e32 v96, v96, v177
	v_sub_f32_e32 v97, v97, v177
	v_exp_f32_e64 v226, -v177
	v_add_f32_e32 v175, v175, v177
	v_sub_f32_e32 v210, 0, v175
	v_mov_b32_e32 v211, v210
	v_mov_b32_e32 v212, v210
	v_mov_b32_e32 v213, v210
	v_mov_b32_e32 v214, v210
	v_mov_b32_e32 v215, v210
	v_mov_b32_e32 v216, v210
	v_mov_b32_e32 v217, v210
	v_mov_b32_e32 v218, v210
	v_mov_b32_e32 v219, v210
	v_mov_b32_e32 v220, v210
	v_mov_b32_e32 v221, v210
	v_mov_b32_e32 v222, v210
	v_mov_b32_e32 v223, v210
	v_mov_b32_e32 v224, v210
	v_mov_b32_e32 v225, v210
	s_branch .Lsm2_join
